# speedup vs baseline: 1.0061x; 1.0061x over previous
.LBB1_7:
	s_or_b64 exec, exec, s[2:3]
	v_mov_b32_e32 v10, v167
	s_waitcnt lgkmcnt(0)
	s_barrier
	s_ashr_i32 s2, s4, 6
	v_ashrrev_i32_e32 v11, 5, v10
	s_waitcnt vmcnt(18)
	v_and_b32_e32 v2, 3, v10
	v_lshlrev_b32_e32 v4, 2, v10
	v_lshl_add_u32 v34, v11, 9, v1
	v_lshlrev_b32_e32 v2, 3, v2
	v_and_b32_e32 v4, 32, v4
	v_and_b32_e32 v3, 16, v10
	v_or3_b32 v2, v34, v2, v4
	v_lshlrev_b32_e32 v4, 4, v10
	s_cmpk_lt_u32 s4, 0x80
	v_and_b32_e32 v4, 64, v4
	v_lshlrev_b32_e32 v3, 3, v3
	s_cselect_b32 s3, 0, 15
	v_or3_b32 v15, v2, v4, v3
	v_bitop3_b32 v2, v10, s3, 15 bitop3:0x6c
	v_lshlrev_b32_e32 v2, 3, v2
	v_or_b32_e32 v3, 0x10800, v2
	v_or_b32_e32 v4, 0x10880, v2
	v_or_b32_e32 v6, 0x10900, v2
	v_or_b32_e32 v8, 0x10980, v2
	ds_read_b64 v[2:3], v3
	ds_read_b64 v[4:5], v4
	ds_read_b64 v[6:7], v6
	ds_read_b64 v[8:9], v8
	v_and_b32_e32 v16, 31, v10
	v_cmp_gt_u32_e32 vcc, 16, v16
	v_lshrrev_b32_e32 v12, 1, v10
	v_lshlrev_b32_e32 v13, 1, v10
	s_waitcnt lgkmcnt(3)
	v_cndmask_b32_e32 v16, v3, v2, vcc
	v_cndmask_b32_e64 v2, v2, -v3, vcc
	s_waitcnt lgkmcnt(2)
	v_cndmask_b32_e64 v3, v4, -v5, vcc
	v_cndmask_b32_e32 v18, v5, v4, vcc
	s_waitcnt lgkmcnt(1)
	v_cndmask_b32_e64 v4, v6, -v7, vcc
	s_waitcnt lgkmcnt(0)
	v_cndmask_b32_e64 v5, v8, -v9, vcc
	v_cvt_pk_f16_f32 v20, v2, v3
	v_lshrrev_b32_e32 v2, 1, v11
	v_cvt_pk_f16_f32 v21, v4, v5
	v_lshrrev_b32_e32 v3, 2, v10
	v_xor_b32_e32 v5, v12, v11
	v_xor_b32_e32 v2, v2, v10
	v_xor_b32_e32 v3, v3, v11
	v_and_b32_e32 v4, 2, v13
	v_lshlrev_b32_e32 v5, 2, v5
	v_lshlrev_b32_e32 v2, 3, v2
	v_bfe_i32 v14, v10, 4, 1
	v_and_b32_e32 v17, 15, v10
	v_and_b32_e32 v5, 4, v5
	v_and_b32_e32 v2, 8, v2
	v_and_or_b32 v3, v3, 1, v4
	v_lshlrev_b32_e32 v4, 8, v11
	s_lshl_b32 s3, s2, 3
	v_cndmask_b32_e32 v19, v7, v6, vcc
	v_or3_b32 v2, v3, v5, v2
	v_lshlrev_b32_e32 v3, 11, v17
	v_and_b32_e32 v5, 0x200, v4
	v_and_b32_e32 v4, 0x100, v4
	v_bitop3_b32 v6, s3, v14, 31 bitop3:0x78
	v_or3_b32 v12, v5, v3, v4
	v_lshlrev_b32_e32 v13, 4, v2
	ds_read2_b64 v[2:5], v15 offset1:32
	v_lshl_add_u32 v6, v6, 3, v34
	v_cndmask_b32_e32 v22, v9, v8, vcc
	ds_read2_b64 v[6:9], v6 offset0:128 offset1:160
	v_cvt_pk_f16_f32 v19, v19, v22
	s_waitcnt lgkmcnt(1)
	v_mov_b32_e32 v24, v3
	v_mov_b32_e32 v25, v5
	v_pk_mov_b32 v[28:29], v[4:5], v[2:3] op_sel:[1,0]
	v_cvt_pk_f16_f32 v18, v16, v18
	v_lshlrev_b32_e32 v16, 11, v10
	v_mov_b32_e32 v22, v2
	v_mov_b32_e32 v23, v4
	s_waitcnt lgkmcnt(0)
	v_pk_mul_f32 v[10:11], v[6:7], v[24:25] op_sel:[1,0]
	v_pk_mov_b32 v[26:27], v[2:3], v[4:5] op_sel:[1,0]
	v_pk_mul_f32 v[2:3], v[6:7], v[28:29]
	v_pk_mul_f32 v[4:5], v[8:9], v[24:25] op_sel:[1,0]
	v_pk_fma_f32 v[10:11], v[6:7], v[22:23], v[10:11] op_sel_hi:[0,1,1] neg_lo:[0,0,1] neg_hi:[0,0,1]
	v_pk_fma_f32 v[2:3], v[6:7], v[26:27], v[2:3] op_sel:[0,0,1] op_sel_hi:[1,1,0]
	v_pk_fma_f32 v[6:7], v[8:9], v[22:23], v[4:5] op_sel_hi:[0,1,1] neg_lo:[0,0,1] neg_hi:[0,0,1]
	v_pk_mul_f32 v[4:5], v[8:9], v[28:29]
	v_and_b32_e32 v36, 31, v14
	v_pk_fma_f32 v[4:5], v[8:9], v[26:27], v[4:5] op_sel:[0,0,1] op_sel_hi:[1,1,0]
	s_and_b32 s5, s3, 8
	v_cvt_pk_f16_f32 v5, v4, v5
	v_cvt_pk_f16_f32 v4, v2, v3
	v_cvt_pk_f16_f32 v3, v6, v7
	v_cvt_pk_f16_f32 v2, v10, v11
	v_and_b32_e32 v6, 0x8000, v16
	v_or3_b32 v35, v13, v12, v6
	v_mfma_f32_32x32x16_f16 v[2:17], v[2:5], v[18:21], 0
	s_bfe_u32 s26, s2, 0x10001
	s_or_b32 s5, s26, s5
	s_lshl_b32 s26, s2, 9
	s_and_b32 s26, s26, 0x400
	s_lshl_b32 s5, s5, 4
	v_mov_b32_e32 v30, s26
	v_bitop3_b32 v37, s5, v35, v30 bitop3:0x36
	s_nop 4
	v_cvt_pk_f16_f32 v9, v8, v9
	v_cvt_pk_f16_f32 v8, v6, v7
	v_cvt_pk_f16_f32 v7, v4, v5
	v_bitop3_b32 v4, s3, v36, 1 bitop3:0x36
	v_lshl_add_u32 v4, v4, 3, v34
	ds_read2_b64 v[30:33], v4 offset0:128 offset1:160
	v_cvt_pk_f16_f32 v6, v2, v3
	ds_write_b128 v37, v[6:9]
	v_cvt_pk_f16_f32 v4, v14, v15
	v_cvt_pk_f16_f32 v5, v16, v17
	s_waitcnt lgkmcnt(1)
	v_pk_mul_f32 v[8:9], v[32:33], v[24:25] op_sel:[1,0]
	v_pk_mul_f32 v[2:3], v[30:31], v[24:25] op_sel:[1,0]
	v_pk_mul_f32 v[6:7], v[30:31], v[28:29]
	v_pk_fma_f32 v[14:15], v[32:33], v[22:23], v[8:9] op_sel_hi:[0,1,1] neg_lo:[0,0,1] neg_hi:[0,0,1]
	v_pk_mul_f32 v[8:9], v[32:33], v[28:29]
	v_pk_fma_f32 v[2:3], v[30:31], v[22:23], v[2:3] op_sel_hi:[0,1,1] neg_lo:[0,0,1] neg_hi:[0,0,1]
	v_pk_fma_f32 v[6:7], v[30:31], v[26:27], v[6:7] op_sel:[0,0,1] op_sel_hi:[1,1,0]
	v_pk_fma_f32 v[8:9], v[32:33], v[26:27], v[8:9] op_sel:[0,0,1] op_sel_hi:[1,1,0]
	v_xor_b32_e32 v38, 16, v37
	v_cvt_pk_f16_f32 v9, v8, v9
	v_cvt_pk_f16_f32 v8, v6, v7
	v_cvt_pk_f16_f32 v7, v14, v15
	v_cvt_pk_f16_f32 v6, v2, v3
	v_cvt_pk_f16_f32 v3, v12, v13
	v_cvt_pk_f16_f32 v2, v10, v11
	v_xor_b32_e32 v10, 0x280, v37
	ds_write_b128 v10, v[2:5]
	v_mfma_f32_32x32x16_f16 v[2:17], v[6:9], v[18:21], 0
	s_or_b32 s28, s5, s26
	s_nop 10
	v_cvt_pk_f16_f32 v9, v8, v9
	v_cvt_pk_f16_f32 v8, v6, v7
	v_cvt_pk_f16_f32 v7, v4, v5
	v_bitop3_b32 v4, s3, v36, 2 bitop3:0x36
	v_lshl_add_u32 v4, v4, 3, v34
	ds_read2_b64 v[30:33], v4 offset0:128 offset1:160
	v_cvt_pk_f16_f32 v6, v2, v3
	ds_write_b128 v38, v[6:9]
	v_cvt_pk_f16_f32 v4, v14, v15
	v_cvt_pk_f16_f32 v5, v16, v17
	s_waitcnt lgkmcnt(1)
	v_pk_mul_f32 v[8:9], v[32:33], v[24:25] op_sel:[1,0]
	v_pk_mul_f32 v[2:3], v[30:31], v[24:25] op_sel:[1,0]
	v_pk_mul_f32 v[6:7], v[30:31], v[28:29]
	v_pk_fma_f32 v[14:15], v[32:33], v[22:23], v[8:9] op_sel_hi:[0,1,1] neg_lo:[0,0,1] neg_hi:[0,0,1]
	v_pk_mul_f32 v[8:9], v[32:33], v[28:29]
	v_pk_fma_f32 v[2:3], v[30:31], v[22:23], v[2:3] op_sel_hi:[0,1,1] neg_lo:[0,0,1] neg_hi:[0,0,1]
	v_pk_fma_f32 v[6:7], v[30:31], v[26:27], v[6:7] op_sel:[0,0,1] op_sel_hi:[1,1,0]
	v_pk_fma_f32 v[8:9], v[32:33], v[26:27], v[8:9] op_sel:[0,0,1] op_sel_hi:[1,1,0]
	v_bitop3_b32 v38, s28, v35, 32 bitop3:0x36
	v_cvt_pk_f16_f32 v9, v8, v9
	v_cvt_pk_f16_f32 v8, v6, v7
	v_cvt_pk_f16_f32 v7, v14, v15
	v_cvt_pk_f16_f32 v6, v2, v3
	v_cvt_pk_f16_f32 v3, v12, v13
	v_cvt_pk_f16_f32 v2, v10, v11
	v_xor_b32_e32 v10, 0x290, v37
	ds_write_b128 v10, v[2:5]
	v_mfma_f32_32x32x16_f16 v[2:17], v[6:9], v[18:21], 0
	s_nop 11
	v_cvt_pk_f16_f32 v9, v8, v9
	v_cvt_pk_f16_f32 v8, v6, v7
	v_cvt_pk_f16_f32 v7, v4, v5
	v_bitop3_b32 v4, s3, v36, 3 bitop3:0x36
	v_lshl_add_u32 v4, v4, 3, v34
	ds_read2_b64 v[30:33], v4 offset0:128 offset1:160
	v_cvt_pk_f16_f32 v6, v2, v3
	ds_write_b128 v38, v[6:9]
	v_cvt_pk_f16_f32 v4, v14, v15
	v_cvt_pk_f16_f32 v5, v16, v17
	s_waitcnt lgkmcnt(1)
	v_pk_mul_f32 v[8:9], v[32:33], v[24:25] op_sel:[1,0]
	v_pk_mul_f32 v[2:3], v[30:31], v[24:25] op_sel:[1,0]
	v_pk_mul_f32 v[6:7], v[30:31], v[28:29]
	v_pk_fma_f32 v[14:15], v[32:33], v[22:23], v[8:9] op_sel_hi:[0,1,1] neg_lo:[0,0,1] neg_hi:[0,0,1]
	v_pk_mul_f32 v[8:9], v[32:33], v[28:29]
	v_pk_fma_f32 v[2:3], v[30:31], v[22:23], v[2:3] op_sel_hi:[0,1,1] neg_lo:[0,0,1] neg_hi:[0,0,1]
	v_pk_fma_f32 v[6:7], v[30:31], v[26:27], v[6:7] op_sel:[0,0,1] op_sel_hi:[1,1,0]
	v_pk_fma_f32 v[8:9], v[32:33], v[26:27], v[8:9] op_sel:[0,0,1] op_sel_hi:[1,1,0]
	s_nop 0
	v_cvt_pk_f16_f32 v9, v8, v9
	v_cvt_pk_f16_f32 v8, v6, v7
	v_cvt_pk_f16_f32 v7, v14, v15
	v_cvt_pk_f16_f32 v6, v2, v3
	v_cvt_pk_f16_f32 v3, v12, v13
	v_cvt_pk_f16_f32 v2, v10, v11
	v_xor_b32_e32 v10, 0x280, v38
	ds_write_b128 v10, v[2:5]
	v_mfma_f32_32x32x16_f16 v[2:17], v[6:9], v[18:21], 0
	v_xor_b32_e32 v38, 48, v37
	s_nop 10
	v_cvt_pk_f16_f32 v9, v8, v9
	v_cvt_pk_f16_f32 v8, v6, v7
	v_cvt_pk_f16_f32 v7, v4, v5
	v_bitop3_b32 v4, s3, v36, 4 bitop3:0x36
	v_lshl_add_u32 v4, v4, 3, v34
	ds_read2_b64 v[30:33], v4 offset0:128 offset1:160
	v_cvt_pk_f16_f32 v6, v2, v3
	ds_write_b128 v38, v[6:9]
	v_cvt_pk_f16_f32 v4, v14, v15
	v_cvt_pk_f16_f32 v5, v16, v17
	s_waitcnt lgkmcnt(1)
	v_pk_mul_f32 v[8:9], v[32:33], v[24:25] op_sel:[1,0]
	v_pk_mul_f32 v[2:3], v[30:31], v[24:25] op_sel:[1,0]
	v_pk_mul_f32 v[6:7], v[30:31], v[28:29]
	v_pk_fma_f32 v[14:15], v[32:33], v[22:23], v[8:9] op_sel_hi:[0,1,1] neg_lo:[0,0,1] neg_hi:[0,0,1]
	v_pk_mul_f32 v[8:9], v[32:33], v[28:29]
	v_pk_fma_f32 v[2:3], v[30:31], v[22:23], v[2:3] op_sel_hi:[0,1,1] neg_lo:[0,0,1] neg_hi:[0,0,1]
	v_pk_fma_f32 v[6:7], v[30:31], v[26:27], v[6:7] op_sel:[0,0,1] op_sel_hi:[1,1,0]
	v_pk_fma_f32 v[8:9], v[32:33], v[26:27], v[8:9] op_sel:[0,0,1] op_sel_hi:[1,1,0]
	v_bitop3_b32 v38, s28, v35, 64 bitop3:0x36
	v_cvt_pk_f16_f32 v9, v8, v9
	v_cvt_pk_f16_f32 v8, v6, v7
	v_cvt_pk_f16_f32 v7, v14, v15
	v_cvt_pk_f16_f32 v6, v2, v3
	v_cvt_pk_f16_f32 v3, v12, v13
	v_cvt_pk_f16_f32 v2, v10, v11
	v_xor_b32_e32 v10, 0x2b0, v37
	ds_write_b128 v10, v[2:5]
	v_mfma_f32_32x32x16_f16 v[2:17], v[6:9], v[18:21], 0
	v_bitop3_b32 v35, s28, v35, v158 bitop3:0x36
	s_nop 10
	v_cvt_pk_f16_f32 v9, v8, v9
	v_cvt_pk_f16_f32 v8, v6, v7
	v_cvt_pk_f16_f32 v7, v4, v5
	v_bitop3_b32 v4, s3, v36, 5 bitop3:0x36
	v_lshl_add_u32 v4, v4, 3, v34
	ds_read2_b64 v[30:33], v4 offset0:128 offset1:160
	v_cvt_pk_f16_f32 v6, v2, v3
	ds_write_b128 v38, v[6:9]
	v_cvt_pk_f16_f32 v4, v14, v15
	v_cvt_pk_f16_f32 v5, v16, v17
	s_waitcnt lgkmcnt(1)
	v_pk_mul_f32 v[8:9], v[32:33], v[24:25] op_sel:[1,0]
	v_pk_mul_f32 v[2:3], v[30:31], v[24:25] op_sel:[1,0]
	v_pk_mul_f32 v[6:7], v[30:31], v[28:29]
	v_pk_fma_f32 v[14:15], v[32:33], v[22:23], v[8:9] op_sel_hi:[0,1,1] neg_lo:[0,0,1] neg_hi:[0,0,1]
	v_pk_mul_f32 v[8:9], v[32:33], v[28:29]
	v_pk_fma_f32 v[2:3], v[30:31], v[22:23], v[2:3] op_sel_hi:[0,1,1] neg_lo:[0,0,1] neg_hi:[0,0,1]
	v_pk_fma_f32 v[6:7], v[30:31], v[26:27], v[6:7] op_sel:[0,0,1] op_sel_hi:[1,1,0]
	v_pk_fma_f32 v[8:9], v[32:33], v[26:27], v[8:9] op_sel:[0,0,1] op_sel_hi:[1,1,0]
	s_nop 0
	v_cvt_pk_f16_f32 v9, v8, v9
	v_cvt_pk_f16_f32 v8, v6, v7
	v_cvt_pk_f16_f32 v7, v14, v15
	v_cvt_pk_f16_f32 v6, v2, v3
	v_cvt_pk_f16_f32 v3, v12, v13
	v_cvt_pk_f16_f32 v2, v10, v11
	v_xor_b32_e32 v10, 0x280, v38
	ds_write_b128 v10, v[2:5]
	v_mfma_f32_32x32x16_f16 v[2:17], v[6:9], v[18:21], 0
	v_xor_b32_e32 v38, 0x50, v37
	s_nop 10
	v_cvt_pk_f16_f32 v9, v8, v9
	v_cvt_pk_f16_f32 v8, v6, v7
	v_cvt_pk_f16_f32 v7, v4, v5
	v_bitop3_b32 v4, s3, v36, 6 bitop3:0x36
	v_lshl_add_u32 v4, v4, 3, v34
	ds_read2_b64 v[30:33], v4 offset0:128 offset1:160
	v_cvt_pk_f16_f32 v6, v2, v3
	ds_write_b128 v38, v[6:9]
	v_cvt_pk_f16_f32 v4, v14, v15
	v_cvt_pk_f16_f32 v5, v16, v17
	s_waitcnt lgkmcnt(1)
	v_pk_mul_f32 v[8:9], v[32:33], v[24:25] op_sel:[1,0]
	v_pk_mul_f32 v[2:3], v[30:31], v[24:25] op_sel:[1,0]
	v_pk_mul_f32 v[6:7], v[30:31], v[28:29]
	v_pk_fma_f32 v[14:15], v[32:33], v[22:23], v[8:9] op_sel_hi:[0,1,1] neg_lo:[0,0,1] neg_hi:[0,0,1]
	v_pk_mul_f32 v[8:9], v[32:33], v[28:29]
	v_pk_fma_f32 v[2:3], v[30:31], v[22:23], v[2:3] op_sel_hi:[0,1,1] neg_lo:[0,0,1] neg_hi:[0,0,1]
	v_pk_fma_f32 v[6:7], v[30:31], v[26:27], v[6:7] op_sel:[0,0,1] op_sel_hi:[1,1,0]
	v_pk_fma_f32 v[8:9], v[32:33], v[26:27], v[8:9] op_sel:[0,0,1] op_sel_hi:[1,1,0]
	s_nop 0
	v_cvt_pk_f16_f32 v9, v8, v9
	v_cvt_pk_f16_f32 v8, v6, v7
	v_cvt_pk_f16_f32 v7, v14, v15
	v_cvt_pk_f16_f32 v6, v2, v3
	v_cvt_pk_f16_f32 v3, v12, v13
	v_cvt_pk_f16_f32 v2, v10, v11
	v_xor_b32_e32 v10, 0x2d0, v37
	ds_write_b128 v10, v[2:5]
	v_mfma_f32_32x32x16_f16 v[2:17], v[6:9], v[18:21], 0
	s_nop 11
	v_cvt_pk_f16_f32 v9, v8, v9
	v_cvt_pk_f16_f32 v8, v6, v7
	v_cvt_pk_f16_f32 v7, v4, v5
	v_bitop3_b32 v4, s3, v36, 7 bitop3:0x36
	v_lshl_add_u32 v4, v4, 3, v34
	ds_read2_b64 v[30:33], v4 offset0:128 offset1:160
	v_cvt_pk_f16_f32 v6, v2, v3
	ds_write_b128 v35, v[6:9]
	v_cvt_pk_f16_f32 v4, v14, v15
	v_cvt_pk_f16_f32 v5, v16, v17
	s_waitcnt lgkmcnt(1)
	v_pk_mul_f32 v[8:9], v[32:33], v[24:25] op_sel:[1,0]
	v_pk_mul_f32 v[2:3], v[30:31], v[24:25] op_sel:[1,0]
	v_pk_mul_f32 v[6:7], v[30:31], v[28:29]
	v_pk_fma_f32 v[14:15], v[32:33], v[22:23], v[8:9] op_sel_hi:[0,1,1] neg_lo:[0,0,1] neg_hi:[0,0,1]
	v_pk_mul_f32 v[8:9], v[32:33], v[28:29]
	v_pk_fma_f32 v[2:3], v[30:31], v[22:23], v[2:3] op_sel_hi:[0,1,1] neg_lo:[0,0,1] neg_hi:[0,0,1]
	v_pk_fma_f32 v[6:7], v[30:31], v[26:27], v[6:7] op_sel:[0,0,1] op_sel_hi:[1,1,0]
	v_pk_fma_f32 v[8:9], v[32:33], v[26:27], v[8:9] op_sel:[0,0,1] op_sel_hi:[1,1,0]
	s_nop 0
	v_cvt_pk_f16_f32 v9, v8, v9
	v_cvt_pk_f16_f32 v8, v6, v7
	v_cvt_pk_f16_f32 v7, v14, v15
	v_cvt_pk_f16_f32 v6, v2, v3
	v_cvt_pk_f16_f32 v3, v12, v13
	v_cvt_pk_f16_f32 v2, v10, v11
	v_xor_b32_e32 v10, 0x280, v35
	ds_write_b128 v10, v[2:5]
	v_mfma_f32_32x32x16_f16 v[2:17], v[6:9], v[18:21], 0
	v_xor_b32_e32 v18, 0x70, v37
	s_nop 10
	v_cvt_pk_f16_f32 v9, v8, v9
	v_cvt_pk_f16_f32 v8, v6, v7
	v_cvt_pk_f16_f32 v7, v4, v5
	v_cvt_pk_f16_f32 v6, v2, v3
	ds_write_b128 v18, v[6:9]
	v_cvt_pk_f16_f32 v5, v16, v17
	v_cvt_pk_f16_f32 v4, v14, v15
	v_cvt_pk_f16_f32 v3, v12, v13
	v_cvt_pk_f16_f32 v2, v10, v11
	v_xor_b32_e32 v6, 0x2f0, v37
	ds_write_b128 v6, v[2:5]
	s_waitcnt lgkmcnt(0)
	s_barrier
	s_setprio 1
	v_lshrrev_b32_e32 v182, 5, v167
	v_bfe_u32 v2, v156, 4, 1
	v_bitop3_b32 v3, v182, v156, 1 bitop3:0x78
	v_lshlrev_b32_e32 v154, 2, v182
	v_xor_b32_e32 v3, v3, v2
	v_bitop3_b32 v4, v154, v156, 4 bitop3:0x78
	v_and_b32_e32 v5, 10, v156
	v_or3_b32 v3, v5, v4, v3
	s_lshl_b32 s5, s2, 4
	v_lshlrev_b32_e32 v3, 4, v3
	s_lshl_b32 s3, s2, 13
	s_and_b32 s29, s5, 16
	v_lshlrev_b32_e32 v170, 8, v182
	v_lshl_or_b32 v171, v2, 10, v3
	s_or_b32 s26, s29, s3
	v_bitop3_b32 v179, v171, s26, v170 bitop3:0x36
	ds_read_b128 v[18:21], v179
	ds_read_b128 v[22:25], v179 offset:32768
	s_waitcnt vmcnt(17) lgkmcnt(1)
	v_mfma_f32_32x32x16_f16 v[2:17], v[18:21], v[150:153], 0
	s_or_b32 s5, s26, 0x280
	v_bitop3_b32 v178, v171, s5, v170 bitop3:0x36
	s_or_b32 s30, s3, 0x800
	s_or_b32 s5, s29, s30
	s_or_b32 s31, s5, 0xa0
	s_or_b32 s5, s5, 0x220
	s_or_b32 s33, s3, 0x1000
	s_waitcnt vmcnt(7)
	v_mfma_f32_32x32x16_f16 v[34:49], v[18:21], v[134:137], 0
	ds_read_b128 v[18:21], v178
	ds_read_b128 v[26:29], v178 offset:32768
	s_or_b32 s29, s29, 64
	s_or_b32 s34, s29, s33
	v_bitop3_b32 v180, v171, s34, v170 bitop3:0x36
	s_or_b32 s29, s3, s29
	s_or_b32 s29, s29, 0x1280
	s_waitcnt lgkmcnt(1)
	v_mfma_f32_32x32x16_f16 v[2:17], v[18:21], v[146:149], v[2:17]
	v_mfma_f32_32x32x16_f16 v[2:17], v[22:25], v[142:145], v[2:17]
	v_mfma_f32_32x32x16_f16 v[34:49], v[18:21], v[126:129], v[34:49]
	s_waitcnt lgkmcnt(0)
	v_mfma_f32_32x32x16_f16 v[2:17], v[26:29], v[138:141], v[2:17]
	v_mfma_f32_32x32x16_f16 v[34:49], v[22:25], v[122:125], v[34:49]
	s_nop 10
	v_cvt_pk_f16_f32 v9, v8, v9
	v_cvt_pk_f16_f32 v8, v6, v7
	v_cvt_pk_f16_f32 v7, v4, v5
	v_cvt_pk_f16_f32 v6, v2, v3
	v_cvt_pk_f16_f32 v5, v16, v17
	v_cvt_pk_f16_f32 v4, v14, v15
	v_cvt_pk_f16_f32 v3, v12, v13
	s_waitcnt vmcnt(5)
	v_mfma_f32_32x32x16_f16 v[34:49], v[26:29], v[130:133], v[34:49]
	v_cvt_pk_f16_f32 v2, v10, v11
	v_mfma_f32_32x32x16_f16 v[18:33], v[6:9], v[118:121], 0
	s_nop 9
	v_cvt_pk_f16_f32 v13, v40, v41
	v_cvt_pk_f16_f32 v12, v38, v39
	v_cvt_pk_f16_f32 v11, v36, v37
	v_cvt_pk_f16_f32 v10, v34, v35
	v_cvt_pk_f16_f32 v17, v48, v49
	v_cvt_pk_f16_f32 v16, v46, v47
	v_cvt_pk_f16_f32 v15, v44, v45
	v_mfma_f32_32x32x16_f16 v[50:65], v[6:9], v[102:105], 0
	v_bitop3_b32 v6, v171, s31, v170 bitop3:0x36
	v_cvt_pk_f16_f32 v14, v42, v43
	v_mfma_f32_32x32x16_f16 v[18:33], v[2:5], v[114:117], v[18:33]
	s_waitcnt vmcnt(4)
	v_mfma_f32_32x32x16_f16 v[50:65], v[2:5], v[98:101], v[50:65]
	ds_read_b128 v[2:5], v6
	ds_read_b128 v[6:9], v6 offset:32768
	v_mfma_f32_32x32x16_f16 v[18:33], v[10:13], v[110:113], v[18:33]
	s_waitcnt vmcnt(3)
	v_mfma_f32_32x32x16_f16 v[50:65], v[10:13], v[94:97], v[50:65]
	s_waitcnt lgkmcnt(1)
	v_mfma_f32_32x32x16_f16 v[34:49], v[2:5], v[150:153], 0
	v_mfma_f32_32x32x16_f16 v[18:33], v[14:17], v[106:109], v[18:33]
	s_waitcnt vmcnt(2)
	v_mfma_f32_32x32x16_f16 v[50:65], v[14:17], v[90:93], v[50:65]
	v_bitop3_b32 v14, v171, s5, v170 bitop3:0x36
	ds_read_b128 v[10:13], v14
	ds_read_b128 v[14:17], v14 offset:32768
	s_and_b32 s5, s2, 1
	s_lshl_b32 s31, s5, 4
	s_or_b32 s2, s31, s3
	v_bitop3_b32 v173, v171, s2, v170 bitop3:0x36
	s_nop 2
	v_cvt_pk_f16_f32 v25, v24, v25
	s_waitcnt lgkmcnt(1)
	v_mfma_f32_32x32x16_f16 v[34:49], v[10:13], v[146:149], v[34:49]
	v_cvt_pk_f16_f32 v24, v22, v23
	v_cvt_pk_f16_f32 v23, v20, v21
	v_cvt_pk_f16_f32 v22, v18, v19
	v_cvt_pk_f16_f32 v21, v32, v33
	v_cvt_pk_f16_f32 v20, v30, v31
	v_cvt_pk_f16_f32 v19, v28, v29
	v_cvt_pk_f16_f32 v18, v26, v27
	v_mfma_f32_32x32x16_f16 v[34:49], v[6:9], v[142:145], v[34:49]
	ds_write_b128 v173, v[22:25]
	v_mfma_f32_32x32x16_f16 v[66:81], v[2:5], v[134:137], 0
	s_waitcnt lgkmcnt(1)
	v_mfma_f32_32x32x16_f16 v[34:49], v[14:17], v[138:141], v[34:49]
	v_mfma_f32_32x32x16_f16 v[66:81], v[10:13], v[126:129], v[66:81]
	s_nop 10
	v_cvt_pk_f16_f32 v41, v40, v41
	v_cvt_pk_f16_f32 v40, v38, v39
	v_cvt_pk_f16_f32 v38, v34, v35
	v_bitop3_b32 v34, v156, 31, v156 bitop3:0xc
	v_cvt_pk_f16_f32 v39, v36, v37
	v_lshrrev_b32_e32 v35, 4, v34
	v_bitop3_b32 v36, v34, v182, 1 bitop3:0x6c
	v_mfma_f32_32x32x16_f16 v[66:81], v[6:9], v[122:125], v[66:81]
	v_xor_b32_e32 v36, v36, v35
	v_bitop3_b32 v34, v34, v154, 4 bitop3:0x6c
	v_bitop3_b32 v37, v156, 10, 31 bitop3:8
	v_or3_b32 v34, v37, v34, v36
	v_lshlrev_b32_e32 v35, 10, v35
	v_lshlrev_b32_e32 v34, 4, v34
	v_or3_b32 v154, v35, v34, v170
	v_bitop3_b32 v172, s2, v154, v159 bitop3:0x36
	ds_write_b128 v172, v[18:21]
	v_cvt_pk_f16_f32 v21, v56, v57
	v_cvt_pk_f16_f32 v20, v54, v55
	v_cvt_pk_f16_f32 v19, v52, v53
	v_cvt_pk_f16_f32 v18, v50, v51
	v_mfma_f32_32x32x16_f16 v[66:81], v[14:17], v[130:133], v[66:81]
	v_cvt_pk_f16_f32 v177, v48, v49
	v_cvt_pk_f16_f32 v176, v46, v47
	v_cvt_pk_f16_f32 v175, v44, v45
	v_cvt_pk_f16_f32 v174, v42, v43
	ds_write_b128 v173, v[18:21] offset:32768
	v_cvt_pk_f16_f32 v21, v64, v65
	v_cvt_pk_f16_f32 v20, v62, v63
	v_mfma_f32_32x32x16_f16 v[2:17], v[38:41], v[118:121], 0
	v_cvt_pk_f16_f32 v19, v60, v61
	v_cvt_pk_f16_f32 v18, v58, v59
	ds_write_b128 v172, v[18:21] offset:32768
	ds_read_b128 v[18:21], v180
	ds_read_b128 v[22:25], v180 offset:32768
	v_cvt_pk_f16_f32 v73, v72, v73
	v_cvt_pk_f16_f32 v72, v70, v71
	v_mfma_f32_32x32x16_f16 v[34:49], v[38:41], v[102:105], 0
	v_cvt_pk_f16_f32 v71, v68, v69
	v_cvt_pk_f16_f32 v70, v66, v67
	v_cvt_pk_f16_f32 v69, v80, v81
	v_cvt_pk_f16_f32 v68, v78, v79
	v_cvt_pk_f16_f32 v67, v76, v77
	v_cvt_pk_f16_f32 v66, v74, v75
	v_mfma_f32_32x32x16_f16 v[2:17], v[174:177], v[114:117], v[2:17]
	v_mfma_f32_32x32x16_f16 v[34:49], v[174:177], v[98:101], v[34:49]
	v_bitop3_b32 v176, v171, s29, v170 bitop3:0x36
	ds_read_b128 v[26:29], v176
	ds_read_b128 v[30:33], v176 offset:32768
	s_or_b32 s29, s31, s30
	s_or_b32 s29, s29, 0xa0
	v_bitop3_b32 v175, v171, s29, v170 bitop3:0x36
	s_or_b32 s29, s2, 0xaa0
	s_xor_b32 s29, s29, 0x80
	s_waitcnt lgkmcnt(3)
	v_mfma_f32_32x32x16_f16 v[50:65], v[18:21], v[150:153], 0
	v_xor_b32_e32 v174, s29, v154
	s_or_b32 s29, s26, 0x18e0
	v_bitop3_b32 v181, v171, s29, v170 bitop3:0x36
	s_or_b32 s29, s26, 0x1a60
	v_bitop3_b32 v177, v171, s29, v170 bitop3:0x36
	s_or_b32 s29, s31, 64
	s_or_b32 s3, s3, s29
	v_mfma_f32_32x32x16_f16 v[2:17], v[70:73], v[110:113], v[2:17]
	s_or_b32 s29, s29, s33
	v_mfma_f32_32x32x16_f16 v[34:49], v[70:73], v[94:97], v[34:49]
	s_waitcnt lgkmcnt(1)
	v_mfma_f32_32x32x16_f16 v[50:65], v[26:29], v[146:149], v[50:65]
	v_mfma_f32_32x32x16_f16 v[2:17], v[66:69], v[106:109], v[2:17]
	v_mfma_f32_32x32x16_f16 v[34:49], v[66:69], v[90:93], v[34:49]
	s_nop 10
	v_cvt_pk_f16_f32 v9, v8, v9
	v_cvt_pk_f16_f32 v8, v6, v7
	v_cvt_pk_f16_f32 v7, v4, v5
	v_cvt_pk_f16_f32 v6, v2, v3
	v_cvt_pk_f16_f32 v5, v16, v17
	v_cvt_pk_f16_f32 v4, v14, v15
	v_cvt_pk_f16_f32 v3, v12, v13
	v_mfma_f32_32x32x16_f16 v[66:81], v[18:21], v[134:137], 0
	v_cvt_pk_f16_f32 v2, v10, v11
	ds_write_b128 v175, v[6:9]
	ds_write_b128 v174, v[2:5]
	v_cvt_pk_f16_f32 v5, v40, v41
	v_cvt_pk_f16_f32 v4, v38, v39
	v_cvt_pk_f16_f32 v3, v36, v37
	v_cvt_pk_f16_f32 v2, v34, v35
	v_mfma_f32_32x32x16_f16 v[50:65], v[22:25], v[142:145], v[50:65]
	ds_write_b128 v175, v[2:5] offset:32768
	v_cvt_pk_f16_f32 v5, v48, v49
	v_cvt_pk_f16_f32 v4, v46, v47
	v_cvt_pk_f16_f32 v3, v44, v45
	v_cvt_pk_f16_f32 v2, v42, v43
	ds_write_b128 v174, v[2:5] offset:32768
	ds_read_b128 v[2:5], v181
	ds_read_b128 v[6:9], v181 offset:32768
	v_mfma_f32_32x32x16_f16 v[66:81], v[26:29], v[126:129], v[66:81]
	ds_read_b128 v[10:13], v177
	ds_read_b128 v[14:17], v177 offset:32768
	s_waitcnt lgkmcnt(8)
	v_mfma_f32_32x32x16_f16 v[50:65], v[30:33], v[138:141], v[50:65]
	v_mfma_f32_32x32x16_f16 v[66:81], v[22:25], v[122:125], v[66:81]
	s_nop 10
	v_cvt_pk_f16_f32 v57, v56, v57
	v_cvt_pk_f16_f32 v56, v54, v55
	v_cvt_pk_f16_f32 v55, v52, v53
	v_cvt_pk_f16_f32 v54, v50, v51
	v_cvt_pk_f16_f32 v187, v64, v65
	v_cvt_pk_f16_f32 v186, v62, v63
	v_cvt_pk_f16_f32 v185, v60, v61
	v_mfma_f32_32x32x16_f16 v[66:81], v[30:33], v[130:133], v[66:81]
	v_cvt_pk_f16_f32 v184, v58, v59
	v_mfma_f32_32x32x16_f16 v[18:33], v[54:57], v[118:121], 0
	s_nop 9
	v_cvt_pk_f16_f32 v73, v72, v73
	v_cvt_pk_f16_f32 v72, v70, v71
	v_cvt_pk_f16_f32 v71, v68, v69
	v_cvt_pk_f16_f32 v70, v66, v67
	v_cvt_pk_f16_f32 v69, v80, v81
	v_cvt_pk_f16_f32 v68, v78, v79
	v_cvt_pk_f16_f32 v67, v76, v77
	v_mfma_f32_32x32x16_f16 v[50:65], v[54:57], v[102:105], 0
	v_cvt_pk_f16_f32 v66, v74, v75
	v_mfma_f32_32x32x16_f16 v[18:33], v[184:187], v[114:117], v[18:33]
	v_mfma_f32_32x32x16_f16 v[50:65], v[184:187], v[98:101], v[50:65]
	s_waitcnt lgkmcnt(3)
	v_mfma_f32_32x32x16_f16 v[34:49], v[2:5], v[150:153], 0
	v_mfma_f32_32x32x16_f16 v[18:33], v[70:73], v[110:113], v[18:33]
	v_mfma_f32_32x32x16_f16 v[50:65], v[70:73], v[94:97], v[50:65]
	s_waitcnt lgkmcnt(1)
	v_mfma_f32_32x32x16_f16 v[34:49], v[10:13], v[146:149], v[34:49]
	v_mfma_f32_32x32x16_f16 v[18:33], v[66:69], v[106:109], v[18:33]
	v_mfma_f32_32x32x16_f16 v[50:65], v[66:69], v[90:93], v[50:65]
	s_nop 10
	v_cvt_pk_f16_f32 v25, v24, v25
	v_cvt_pk_f16_f32 v24, v22, v23
	v_cvt_pk_f16_f32 v23, v20, v21
	v_cvt_pk_f16_f32 v22, v18, v19
	v_cvt_pk_f16_f32 v21, v32, v33
	v_cvt_pk_f16_f32 v20, v30, v31
	v_cvt_pk_f16_f32 v19, v28, v29
	v_mfma_f32_32x32x16_f16 v[66:81], v[2:5], v[134:137], 0
	v_cvt_pk_f16_f32 v18, v26, v27
	v_cvt_pk_f16_f32 v57, v56, v57
	v_cvt_pk_f16_f32 v56, v54, v55
	v_cvt_pk_f16_f32 v55, v52, v53
	v_cvt_pk_f16_f32 v54, v50, v51
	v_and_b32_e32 v134, 1, v156
	v_mfma_f32_32x32x16_f16 v[34:49], v[6:9], v[142:145], v[34:49]
	v_mfma_f32_32x32x16_f16 v[66:81], v[10:13], v[126:129], v[66:81]
	s_waitcnt lgkmcnt(0)
	v_mfma_f32_32x32x16_f16 v[34:49], v[14:17], v[138:141], v[34:49]
	v_mfma_f32_32x32x16_f16 v[66:81], v[6:9], v[122:125], v[66:81]
	s_nop 10
	v_cvt_pk_f16_f32 v41, v40, v41
	v_cvt_pk_f16_f32 v40, v38, v39
	v_cvt_pk_f16_f32 v39, v36, v37
	v_cvt_pk_f16_f32 v38, v34, v35
	v_cvt_pk_f16_f32 v37, v48, v49
	v_cvt_pk_f16_f32 v36, v46, v47
	v_cvt_pk_f16_f32 v35, v44, v45
	v_mfma_f32_32x32x16_f16 v[66:81], v[14:17], v[130:133], v[66:81]
	v_bitop3_b32 v132, v171, s29, v170 bitop3:0x36
	v_bitop3_b32 v131, s3, v154, v160 bitop3:0x36
	ds_write_b128 v132, v[22:25]
	ds_write_b128 v131, v[18:21]
	v_cvt_pk_f16_f32 v34, v42, v43
	s_or_b32 s3, s2, 0x18e0
	s_or_b32 s2, s2, 0x1ae0
	v_mfma_f32_32x32x16_f16 v[2:17], v[38:41], v[118:121], 0
	s_nop 3
	v_cvt_pk_f16_f32 v45, v72, v73
	v_cvt_pk_f16_f32 v44, v70, v71
	v_cvt_pk_f16_f32 v43, v68, v69
	v_cvt_pk_f16_f32 v42, v66, v67
	v_cvt_pk_f16_f32 v49, v80, v81
	v_cvt_pk_f16_f32 v48, v78, v79
	v_cvt_pk_f16_f32 v47, v76, v77
	v_mfma_f32_32x32x16_f16 v[18:33], v[38:41], v[102:105], 0
	v_cvt_pk_f16_f32 v46, v74, v75
	s_xor_b32 s2, s2, 0x80
	v_cvt_pk_f16_f32 v41, v64, v65
	v_cvt_pk_f16_f32 v40, v62, v63
	v_cvt_pk_f16_f32 v39, v60, v61
	v_cvt_pk_f16_f32 v38, v58, v59
	v_bitop3_b32 v135, v171, s3, v170 bitop3:0x36
	v_mfma_f32_32x32x16_f16 v[2:17], v[34:37], v[114:117], v[2:17]
	v_xor_b32_e32 v133, s2, v154
	ds_write_b128 v132, v[54:57] offset:32768
	ds_write_b128 v131, v[38:41] offset:32768
	v_and_b32_e32 v130, 4, v156
	v_mfma_f32_32x32x16_f16 v[18:33], v[34:37], v[98:101], v[18:33]
	v_mfma_f32_32x32x16_f16 v[2:17], v[42:45], v[110:113], v[2:17]
	v_mfma_f32_32x32x16_f16 v[18:33], v[42:45], v[94:97], v[18:33]
	v_mfma_f32_32x32x16_f16 v[2:17], v[46:49], v[106:109], v[2:17]
	v_mfma_f32_32x32x16_f16 v[18:33], v[46:49], v[90:93], v[18:33]
	s_nop 10
	v_cvt_pk_f16_f32 v9, v8, v9
	v_cvt_pk_f16_f32 v8, v6, v7
	v_cvt_pk_f16_f32 v7, v4, v5
	v_cvt_pk_f16_f32 v6, v2, v3
	v_cvt_pk_f16_f32 v5, v16, v17
	v_cvt_pk_f16_f32 v4, v14, v15
	v_cvt_pk_f16_f32 v3, v12, v13
	v_cvt_pk_f16_f32 v2, v10, v11
	ds_write_b128 v135, v[6:9]
	ds_write_b128 v133, v[2:5]
	v_cvt_pk_f16_f32 v5, v24, v25
	v_cvt_pk_f16_f32 v4, v22, v23
	v_cvt_pk_f16_f32 v3, v20, v21
	v_cvt_pk_f16_f32 v2, v18, v19
	ds_write_b128 v135, v[2:5] offset:32768
	v_cvt_pk_f16_f32 v5, v32, v33
	v_cvt_pk_f16_f32 v4, v30, v31
	v_cvt_pk_f16_f32 v3, v28, v29
	v_cvt_pk_f16_f32 v2, v26, v27
	ds_write_b128 v133, v[2:5] offset:32768
	s_setprio 0
	s_lshl_b32 s2, s27, 3
	s_lshl_b32 s3, s5, 2
	s_or_b32 s2, s3, s2
	s_ashr_i32 s3, s2, 31
	s_lshl_b64 s[2:3], s[2:3], 13
	s_add_u32 s2, s20, s2
	s_addc_u32 s3, s21, s3
	v_lshlrev_b32_e32 v154, 1, v169
	v_lshl_add_u64 v[2:3], s[2:3], 0, v[154:155]
	v_add_co_u32_e32 v2, vcc, s23, v2
	s_waitcnt lgkmcnt(0)
	s_nop 0
	v_addc_co_u32_e32 v3, vcc, 0, v3, vcc
	s_barrier
	global_load_dwordx4 v[62:65], v154, s[2:3]
	global_load_dwordx4 v[46:49], v154, s[2:3] offset:1024
	global_load_dwordx4 v[42:45], v154, s[2:3] offset:2048
	global_load_dwordx4 v[38:41], v154, s[2:3] offset:3072
	global_load_dwordx4 v[54:57], v[2:3], off offset:1024
	global_load_dwordx4 v[50:53], v[2:3], off offset:2048
	v_lshl_add_u64 v[4:5], s[12:13], 0, v[154:155]
	global_load_dwordx4 v[126:129], v154, s[12:13]
	global_load_dwordx4 v[122:125], v154, s[12:13] offset:1024
	global_load_dwordx4 v[118:121], v154, s[12:13] offset:2048
	global_load_dwordx4 v[114:117], v154, s[12:13] offset:3072
	global_load_dwordx4 v[34:37], v168, s[2:3]
	global_load_dwordx4 v[110:113], v168, s[12:13]
	v_add_co_u32_e32 v4, vcc, s23, v4
	s_nop 1
	v_addc_co_u32_e32 v5, vcc, 0, v5, vcc
	global_load_dwordx4 v[58:61], v[2:3], off offset:3072
	global_load_dwordx4 v[106:109], v[4:5], off offset:1024
	global_load_dwordx4 v[94:97], v[4:5], off offset:2048
	global_load_dwordx4 v[90:93], v[4:5], off offset:3072
	v_bfrev_b32_e32 v3, v156
	v_lshlrev_b32_e32 v7, 5, v167
	v_lshlrev_b32_e32 v6, 9, v167
	v_and_b32_e32 v7, 0x200, v7
	v_lshlrev_b32_e32 v8, 8, v167
	v_lshrrev_b32_e32 v3, 27, v3
	v_lshrrev_b32_e32 v2, 2, v167
	v_lshrrev_b32_e32 v4, 4, v156
	v_xor_b32_e32 v5, v169, v156
	v_and_b32_e32 v6, 0x5800, v6
	v_and_b32_e32 v3, 8, v3
	v_and_or_b32 v7, v8, s24, v7
	v_lshrrev_b32_e32 v5, 1, v5
	v_xor_b32_e32 v4, v2, v4
	v_or3_b32 v3, v7, v6, v3
	v_bitop3_b32 v7, v2, v182, 1 bitop3:0x6c
	v_lshlrev_b32_e32 v2, 1, v167
	v_and_b32_e32 v5, 4, v5
	v_lshlrev_b32_e32 v4, 3, v4
	v_lshrrev_b32_e32 v6, 1, v167
	v_and_b32_e32 v2, 2, v2
	v_and_or_b32 v9, v169, 8, v2
	v_and_b32_e32 v2, 8, v4
	v_and_or_b32 v4, v6, 2, v5
	v_or3_b32 v2, v4, v2, v134
	v_lshlrev_b32_e32 v2, 4, v2
	v_bitop3_b32 v146, v3, s28, v2 bitop3:0x36
	v_xor_b32_e32 v8, v6, v182
	v_xor_b32_e32 v147, 0x2010, v146
	ds_read_b64_tr_b16 v[2:3], v146
	ds_read_b64_tr_b16 v[4:5], v147
	v_lshlrev_b32_e32 v8, 2, v8
	v_and_b32_e32 v8, 4, v8
	v_or3_b32 v6, v9, v7, v8
	v_lshlrev_b32_e32 v7, 11, v167
	v_and_b32_e32 v8, 0x7800, v7
	v_lshlrev_b32_e32 v6, 4, v6
	v_or3_b32 v22, v6, v8, v170
	v_and_b32_e32 v23, 0x8000, v7
	s_waitcnt vmcnt(17) lgkmcnt(0)
	v_mfma_f32_32x32x16_f16 v[2:17], v[2:5], v[86:89], 0
	ds_read_b64_tr_b16 v[20:21], v147 offset:32768
	ds_read_b64_tr_b16 v[18:19], v146 offset:32768
	v_xor_b32_e32 v150, 16, v146
	v_xad_u32 v70, v22, s28, v23
	v_xor_b32_e32 v151, 0x2000, v146
	ds_read_b64_tr_b16 v[22:23], v150
	ds_read_b64_tr_b16 v[24:25], v151
	ds_read_b64_tr_b16 v[28:29], v151 offset:32768
	ds_read_b64_tr_b16 v[26:27], v150 offset:32768
	v_xor_b32_e32 v30, 0x280, v70
	v_xor_b32_e32 v148, 32, v146
	s_waitcnt vmcnt(16) lgkmcnt(4)
	v_mfma_f32_32x32x16_f16 v[2:17], v[18:21], v[82:85], v[2:17]
	v_xor_b32_e32 v149, 0x2030, v146
	v_xor_b32_e32 v144, 48, v146
	v_xor_b32_e32 v145, 0x2020, v146
	v_xor_b32_e32 v142, 64, v146
	v_xor_b32_e32 v143, 0x2050, v146
	v_xor_b32_e32 v140, 0x50, v146
	v_xor_b32_e32 v141, 0x2040, v146
	s_nop 4
	v_cvt_pk_f16_f32 v9, v8, v9
	v_cvt_pk_f16_f32 v8, v6, v7
	v_cvt_pk_f16_f32 v7, v4, v5
	v_cvt_pk_f16_f32 v6, v2, v3
	ds_write_b128 v70, v[6:9]
	v_cvt_pk_f16_f32 v21, v16, v17
	v_cvt_pk_f16_f32 v20, v14, v15
	v_cvt_pk_f16_f32 v19, v12, v13
	v_cvt_pk_f16_f32 v18, v10, v11
	s_waitcnt lgkmcnt(3)
	v_mfma_f32_32x32x16_f16 v[2:17], v[22:25], v[86:89], 0
	ds_write_b128 v30, v[18:21]
	ds_read_b64_tr_b16 v[18:19], v148
	ds_read_b64_tr_b16 v[20:21], v149
	ds_read_b64_tr_b16 v[24:25], v149 offset:32768
	ds_read_b64_tr_b16 v[22:23], v148 offset:32768
	v_xor_b32_e32 v30, 0x290, v70
	v_xor_b32_e32 v138, 0x60, v146
	v_xor_b32_e32 v139, 0x2070, v146
	v_xor_b32_e32 v136, 0x70, v146
	v_xor_b32_e32 v137, 0x2060, v146
	s_waitcnt lgkmcnt(6)
	v_mfma_f32_32x32x16_f16 v[2:17], v[26:29], v[82:85], v[2:17]
	v_xor_b32_e32 v26, 16, v70
	v_xor_b32_e32 v71, 0x60, v70
	s_lshl_b64 s[0:1], s[0:1], 13
	s_add_u32 s0, s8, s0
	s_addc_u32 s1, s9, s1
	s_nop 6
	v_cvt_pk_f16_f32 v9, v8, v9
	v_cvt_pk_f16_f32 v8, v6, v7
	v_cvt_pk_f16_f32 v7, v4, v5
	v_cvt_pk_f16_f32 v6, v2, v3
	ds_write_b128 v26, v[6:9]
	v_cvt_pk_f16_f32 v29, v16, v17
	v_cvt_pk_f16_f32 v28, v14, v15
	v_cvt_pk_f16_f32 v27, v12, v13
	v_cvt_pk_f16_f32 v26, v10, v11
	s_waitcnt lgkmcnt(3)
	v_mfma_f32_32x32x16_f16 v[2:17], v[18:21], v[86:89], 0
	ds_write_b128 v30, v[26:29]
	ds_read_b64_tr_b16 v[18:19], v144
	ds_read_b64_tr_b16 v[20:21], v145
	ds_read_b64_tr_b16 v[28:29], v145 offset:32768
	ds_read_b64_tr_b16 v[26:27], v144 offset:32768
	v_xor_b32_e32 v30, 0x2a0, v70
	s_waitcnt lgkmcnt(6)
	v_mfma_f32_32x32x16_f16 v[2:17], v[22:25], v[82:85], v[2:17]
	v_xor_b32_e32 v22, 32, v70
	s_nop 10
	v_cvt_pk_f16_f32 v9, v8, v9
	v_cvt_pk_f16_f32 v8, v6, v7
	v_cvt_pk_f16_f32 v7, v4, v5
	v_cvt_pk_f16_f32 v6, v2, v3
	ds_write_b128 v22, v[6:9]
	v_cvt_pk_f16_f32 v25, v16, v17
	v_cvt_pk_f16_f32 v24, v14, v15
	v_cvt_pk_f16_f32 v23, v12, v13
	v_cvt_pk_f16_f32 v22, v10, v11
	s_waitcnt lgkmcnt(3)
	v_mfma_f32_32x32x16_f16 v[2:17], v[18:21], v[86:89], 0
	ds_write_b128 v30, v[22:25]
	ds_read_b64_tr_b16 v[18:19], v142
	ds_read_b64_tr_b16 v[20:21], v143
	ds_read_b64_tr_b16 v[24:25], v143 offset:32768
	ds_read_b64_tr_b16 v[22:23], v142 offset:32768
	v_xor_b32_e32 v30, 0x2b0, v70
	s_waitcnt lgkmcnt(6)
	v_mfma_f32_32x32x16_f16 v[2:17], v[26:29], v[82:85], v[2:17]
	v_xor_b32_e32 v26, 48, v70
	s_nop 10
	v_cvt_pk_f16_f32 v9, v8, v9
	v_cvt_pk_f16_f32 v8, v6, v7
	v_cvt_pk_f16_f32 v7, v4, v5
	v_cvt_pk_f16_f32 v6, v2, v3
	ds_write_b128 v26, v[6:9]
	v_cvt_pk_f16_f32 v29, v16, v17
	v_cvt_pk_f16_f32 v28, v14, v15
	v_cvt_pk_f16_f32 v27, v12, v13
	v_cvt_pk_f16_f32 v26, v10, v11
	s_waitcnt lgkmcnt(3)
	v_mfma_f32_32x32x16_f16 v[2:17], v[18:21], v[86:89], 0
	ds_write_b128 v30, v[26:29]
	ds_read_b64_tr_b16 v[18:19], v140
	ds_read_b64_tr_b16 v[20:21], v141
	ds_read_b64_tr_b16 v[28:29], v141 offset:32768
	ds_read_b64_tr_b16 v[26:27], v140 offset:32768
	s_waitcnt lgkmcnt(6)
	v_mfma_f32_32x32x16_f16 v[2:17], v[22:25], v[82:85], v[2:17]
	v_xor_b32_e32 v22, 64, v70
	s_nop 10
	v_cvt_pk_f16_f32 v9, v8, v9
	v_cvt_pk_f16_f32 v8, v6, v7
	v_cvt_pk_f16_f32 v7, v4, v5
	v_cvt_pk_f16_f32 v6, v2, v3
	ds_write_b128 v22, v[6:9]
	v_cvt_pk_f16_f32 v5, v16, v17
	v_cvt_pk_f16_f32 v4, v14, v15
	v_cvt_pk_f16_f32 v3, v12, v13
	v_cvt_pk_f16_f32 v2, v10, v11
	s_waitcnt lgkmcnt(3)
	v_mfma_f32_32x32x16_f16 v[10:25], v[18:21], v[86:89], 0
	v_xor_b32_e32 v6, 0x2c0, v70
	ds_write_b128 v6, v[2:5]
	ds_read_b64_tr_b16 v[2:3], v138
	ds_read_b64_tr_b16 v[4:5], v139
	ds_read_b64_tr_b16 v[32:33], v139 offset:32768
	ds_read_b64_tr_b16 v[30:31], v138 offset:32768
	s_waitcnt lgkmcnt(6)
	v_mfma_f32_32x32x16_f16 v[10:25], v[26:29], v[82:85], v[10:25]
	v_xor_b32_e32 v26, 0x50, v70
	s_nop 10
	v_cvt_pk_f16_f32 v9, v16, v17
	v_cvt_pk_f16_f32 v8, v14, v15
	v_cvt_pk_f16_f32 v7, v12, v13
	v_cvt_pk_f16_f32 v6, v10, v11
	ds_write_b128 v26, v[6:9]
	s_waitcnt lgkmcnt(3)
	v_mfma_f32_32x32x16_f16 v[2:17], v[2:5], v[86:89], 0
	v_cvt_pk_f16_f32 v25, v24, v25
	v_cvt_pk_f16_f32 v24, v22, v23
	v_cvt_pk_f16_f32 v23, v20, v21
	v_cvt_pk_f16_f32 v22, v18, v19
	v_xor_b32_e32 v18, 0x2d0, v70
	ds_write_b128 v18, v[22:25]
	ds_read_b64_tr_b16 v[18:19], v136
	ds_read_b64_tr_b16 v[20:21], v137
	s_waitcnt lgkmcnt(4)
	v_mfma_f32_32x32x16_f16 v[2:17], v[30:33], v[82:85], v[2:17]
	ds_read_b64_tr_b16 v[68:69], v137 offset:32768
	ds_read_b64_tr_b16 v[66:67], v136 offset:32768
	s_waitcnt lgkmcnt(2)
	v_mfma_f32_32x32x16_f16 v[18:33], v[18:21], v[86:89], 0
	s_nop 7
	v_cvt_pk_f16_f32 v9, v8, v9
	v_cvt_pk_f16_f32 v8, v6, v7
	v_cvt_pk_f16_f32 v7, v4, v5
	v_cvt_pk_f16_f32 v6, v2, v3
	ds_write_b128 v71, v[6:9]
	v_cvt_pk_f16_f32 v5, v16, v17
	v_cvt_pk_f16_f32 v4, v14, v15
	s_waitcnt lgkmcnt(1)
	v_mfma_f32_32x32x16_f16 v[18:33], v[66:69], v[82:85], v[18:33]
	v_cvt_pk_f16_f32 v3, v12, v13
	v_cvt_pk_f16_f32 v2, v10, v11
	v_xor_b32_e32 v6, 0x2e0, v70
	ds_write_b128 v6, v[2:5]
	v_xor_b32_e32 v6, 0x70, v70
	s_nop 6
	v_cvt_pk_f16_f32 v5, v24, v25
	v_cvt_pk_f16_f32 v4, v22, v23
	v_cvt_pk_f16_f32 v3, v20, v21
	v_cvt_pk_f16_f32 v2, v18, v19
	ds_write_b128 v6, v[2:5]
	v_cvt_pk_f16_f32 v5, v32, v33
	v_cvt_pk_f16_f32 v4, v30, v31
	v_cvt_pk_f16_f32 v3, v28, v29
	v_cvt_pk_f16_f32 v2, v26, v27
	v_xor_b32_e32 v6, 0x2f0, v70
	ds_write_b128 v6, v[2:5]
	v_lshl_add_u64 v[2:3], s[0:1], 0, v[154:155]
	v_lshl_add_u64 v[4:5], v[2:3], 0, s[18:19]
	v_add_co_u32_e32 v2, vcc, s25, v2
	s_waitcnt lgkmcnt(0)
	s_nop 0
	v_addc_co_u32_e32 v3, vcc, 0, v3, vcc
	s_barrier
	global_load_dwordx4 v[102:105], v[2:3], off
	global_load_dwordx4 v[98:101], v[4:5], off offset:1024
	s_setprio 1
	s_add_u32 s0, s2, 0x2000
	s_addc_u32 s1, s3, 0
	v_lshl_add_u64 v[2:3], s[0:1], 0, v[154:155]
	v_add_co_u32_e32 v2, vcc, s23, v2
	global_load_dwordx4 v[66:69], v154, s[0:1]
	global_load_dwordx4 v[70:73], v154, s[0:1] offset:1024
	global_load_dwordx4 v[74:77], v154, s[0:1] offset:2048
	global_load_dwordx4 v[78:81], v154, s[0:1] offset:3072
	v_addc_co_u32_e32 v3, vcc, 0, v3, vcc
	global_load_dwordx4 v[82:85], v168, s[0:1]
	global_load_dwordx4 v[86:89], v[2:3], off offset:1024
	global_load_dwordx4 v[182:185], v[2:3], off offset:2048
	global_load_dwordx4 v[186:189], v[2:3], off offset:3072
	ds_read_b128 v[18:21], v179
	ds_read_b128 v[22:25], v179 offset:32768
	ds_read_b128 v[26:29], v178
	ds_read_b128 v[30:33], v178 offset:32768
	s_add_u32 s0, s2, 0x6000
	s_addc_u32 s1, s3, 0
	s_waitcnt vmcnt(25) lgkmcnt(3)
	v_mfma_f32_32x32x16_f16 v[2:17], v[18:21], v[62:65], 0
	s_add_u32 s2, s2, 0x4000
	s_addc_u32 s3, s3, 0
	s_or_b32 s27, s26, 0x8a0
	s_or_b32 s26, s26, 0xa20
	s_waitcnt vmcnt(24) lgkmcnt(1)
	v_mfma_f32_32x32x16_f16 v[2:17], v[26:29], v[46:49], v[2:17]
	s_waitcnt vmcnt(23)
	v_mfma_f32_32x32x16_f16 v[2:17], v[22:25], v[42:45], v[2:17]
	s_waitcnt vmcnt(22) lgkmcnt(0)
	v_mfma_f32_32x32x16_f16 v[2:17], v[30:33], v[38:41], v[2:17]
	s_waitcnt vmcnt(15)
	v_mfma_f32_32x32x16_f16 v[34:49], v[18:21], v[34:37], 0
	s_nop 9
	v_cvt_pk_f16_f32 v9, v8, v9
	v_cvt_pk_f16_f32 v8, v6, v7
	v_cvt_pk_f16_f32 v7, v4, v5
	v_cvt_pk_f16_f32 v6, v2, v3
	v_cvt_pk_f16_f32 v5, v16, v17
	v_cvt_pk_f16_f32 v4, v14, v15
	v_cvt_pk_f16_f32 v3, v12, v13
	v_mfma_f32_32x32x16_f16 v[34:49], v[26:29], v[54:57], v[34:49]
	v_cvt_pk_f16_f32 v2, v10, v11
	v_mfma_f32_32x32x16_f16 v[34:49], v[22:25], v[50:53], v[34:49]
	s_waitcnt vmcnt(13)
	v_mfma_f32_32x32x16_f16 v[34:49], v[30:33], v[58:61], v[34:49]
	v_mfma_f32_32x32x16_f16 v[18:33], v[6:9], v[126:129], 0
	s_nop 10
	v_cvt_pk_f16_f32 v13, v40, v41
	v_cvt_pk_f16_f32 v12, v38, v39
	v_cvt_pk_f16_f32 v11, v36, v37
	v_cvt_pk_f16_f32 v10, v34, v35
	v_cvt_pk_f16_f32 v17, v48, v49
	v_cvt_pk_f16_f32 v16, v46, v47
	v_cvt_pk_f16_f32 v15, v44, v45
	v_mfma_f32_32x32x16_f16 v[50:65], v[6:9], v[110:113], 0
	v_bitop3_b32 v6, v171, s27, v170 bitop3:0x36
	v_cvt_pk_f16_f32 v14, v42, v43
	v_mfma_f32_32x32x16_f16 v[18:33], v[2:5], v[122:125], v[18:33]
	s_waitcnt vmcnt(12)
	v_mfma_f32_32x32x16_f16 v[50:65], v[2:5], v[106:109], v[50:65]
	ds_read_b128 v[2:5], v6
	ds_read_b128 v[6:9], v6 offset:32768
	v_mfma_f32_32x32x16_f16 v[18:33], v[10:13], v[118:121], v[18:33]
	s_waitcnt vmcnt(11)
	v_mfma_f32_32x32x16_f16 v[50:65], v[10:13], v[94:97], v[50:65]
	s_waitcnt vmcnt(7) lgkmcnt(1)
	v_mfma_f32_32x32x16_f16 v[34:49], v[2:5], v[66:69], 0
	v_mfma_f32_32x32x16_f16 v[18:33], v[14:17], v[114:117], v[18:33]
	v_mfma_f32_32x32x16_f16 v[50:65], v[14:17], v[90:93], v[50:65]
	v_bitop3_b32 v14, v171, s26, v170 bitop3:0x36
	ds_read_b128 v[10:13], v14
	ds_read_b128 v[14:17], v14 offset:32768
	s_nop 7
	v_cvt_pk_f16_f32 v25, v24, v25
	v_cvt_pk_f16_f32 v24, v22, v23
	v_cvt_pk_f16_f32 v23, v20, v21
	v_cvt_pk_f16_f32 v22, v18, v19
	v_cvt_pk_f16_f32 v21, v32, v33
	s_waitcnt vmcnt(6) lgkmcnt(1)
	v_mfma_f32_32x32x16_f16 v[34:49], v[10:13], v[70:73], v[34:49]
	v_cvt_pk_f16_f32 v20, v30, v31
	v_cvt_pk_f16_f32 v19, v28, v29
	v_cvt_pk_f16_f32 v18, v26, v27
	ds_write_b128 v173, v[22:25]
	ds_write_b128 v172, v[18:21]
	v_cvt_pk_f16_f32 v21, v56, v57
	v_cvt_pk_f16_f32 v20, v54, v55
	s_waitcnt vmcnt(5)
	v_mfma_f32_32x32x16_f16 v[34:49], v[6:9], v[74:77], v[34:49]
	v_cvt_pk_f16_f32 v19, v52, v53
	v_cvt_pk_f16_f32 v18, v50, v51
	ds_write_b128 v173, v[18:21] offset:32768
	v_cvt_pk_f16_f32 v21, v64, v65
	v_cvt_pk_f16_f32 v20, v62, v63
	v_cvt_pk_f16_f32 v19, v60, v61
	v_cvt_pk_f16_f32 v18, v58, v59
	s_waitcnt vmcnt(4) lgkmcnt(3)
	v_mfma_f32_32x32x16_f16 v[34:49], v[14:17], v[78:81], v[34:49]
	ds_write_b128 v172, v[18:21] offset:32768
	s_waitcnt vmcnt(3)
	v_mfma_f32_32x32x16_f16 v[66:81], v[2:5], v[82:85], 0
	s_nop 8
	v_cvt_pk_f16_f32 v41, v40, v41
	v_cvt_pk_f16_f32 v40, v38, v39
	v_cvt_pk_f16_f32 v39, v36, v37
	v_cvt_pk_f16_f32 v38, v34, v35
	v_cvt_pk_f16_f32 v85, v48, v49
	v_cvt_pk_f16_f32 v84, v46, v47
	v_cvt_pk_f16_f32 v83, v44, v45
	s_waitcnt vmcnt(2)
	v_mfma_f32_32x32x16_f16 v[66:81], v[10:13], v[86:89], v[66:81]
	v_cvt_pk_f16_f32 v82, v42, v43
	s_waitcnt vmcnt(1)
	v_mfma_f32_32x32x16_f16 v[66:81], v[6:9], v[182:185], v[66:81]
	s_waitcnt vmcnt(0)
	v_mfma_f32_32x32x16_f16 v[66:81], v[14:17], v[186:189], v[66:81]
	v_mfma_f32_32x32x16_f16 v[2:17], v[38:41], v[126:129], 0
	s_nop 10
	v_cvt_pk_f16_f32 v73, v72, v73
	v_cvt_pk_f16_f32 v72, v70, v71
	v_cvt_pk_f16_f32 v70, v66, v67
	v_cvt_pk_f16_f32 v67, v76, v77
	v_cvt_pk_f16_f32 v66, v74, v75
	global_load_dwordx4 v[74:77], v154, s[2:3]
	v_cvt_pk_f16_f32 v71, v68, v69
	v_cvt_pk_f16_f32 v69, v80, v81
	v_cvt_pk_f16_f32 v68, v78, v79
	global_load_dwordx4 v[78:81], v154, s[2:3] offset:1024
	ds_read_b128 v[18:21], v180
	ds_read_b128 v[22:25], v176
	ds_read_b128 v[26:29], v180 offset:32768
	global_load_dwordx4 v[30:33], v154, s[2:3] offset:2048
	v_mfma_f32_32x32x16_f16 v[34:49], v[38:41], v[110:113], 0
	v_mfma_f32_32x32x16_f16 v[2:17], v[82:85], v[122:125], v[2:17]
	v_mfma_f32_32x32x16_f16 v[34:49], v[82:85], v[106:109], v[34:49]
	ds_read_b128 v[82:85], v176 offset:32768
	s_waitcnt vmcnt(2) lgkmcnt(3)
	v_mfma_f32_32x32x16_f16 v[50:65], v[18:21], v[74:77], 0
	v_mfma_f32_32x32x16_f16 v[2:17], v[70:73], v[118:121], v[2:17]
	v_mfma_f32_32x32x16_f16 v[34:49], v[70:73], v[94:97], v[34:49]
	v_lshl_add_u64 v[70:71], s[2:3], 0, v[154:155]
	v_add_co_u32_e32 v152, vcc, s23, v70
	s_nop 1
	v_addc_co_u32_e32 v153, vcc, 0, v71, vcc
	s_waitcnt vmcnt(1) lgkmcnt(2)
	v_mfma_f32_32x32x16_f16 v[50:65], v[22:25], v[78:81], v[50:65]
	v_mfma_f32_32x32x16_f16 v[2:17], v[66:69], v[114:117], v[2:17]
	v_mfma_f32_32x32x16_f16 v[34:49], v[66:69], v[90:93], v[34:49]
	global_load_dwordx4 v[66:69], v154, s[2:3] offset:3072
	s_nop 9
	v_cvt_pk_f16_f32 v9, v8, v9
	v_cvt_pk_f16_f32 v8, v6, v7
	v_cvt_pk_f16_f32 v7, v4, v5
	v_cvt_pk_f16_f32 v6, v2, v3
	v_cvt_pk_f16_f32 v5, v16, v17
	v_cvt_pk_f16_f32 v4, v14, v15
	s_waitcnt vmcnt(1) lgkmcnt(1)
	v_mfma_f32_32x32x16_f16 v[50:65], v[26:29], v[30:33], v[50:65]
	global_load_dwordx4 v[30:33], v168, s[2:3]
	global_load_dwordx4 v[86:89], v[152:153], off offset:1024
	s_nop 0
	global_load_dwordx4 v[168:171], v168, s[0:1]
	v_cvt_pk_f16_f32 v3, v12, v13
	v_cvt_pk_f16_f32 v2, v10, v11
	ds_write_b128 v175, v[6:9]
	ds_write_b128 v174, v[2:5]
	v_cvt_pk_f16_f32 v5, v40, v41
	s_waitcnt vmcnt(3) lgkmcnt(2)
	v_mfma_f32_32x32x16_f16 v[50:65], v[82:85], v[66:69], v[50:65]
	global_load_dwordx4 v[182:185], v154, s[0:1] offset:1024
	v_cvt_pk_f16_f32 v4, v38, v39
	v_cvt_pk_f16_f32 v3, v36, v37
	v_cvt_pk_f16_f32 v2, v34, v35
	ds_write_b128 v175, v[2:5] offset:32768
	v_cvt_pk_f16_f32 v5, v48, v49
	v_cvt_pk_f16_f32 v4, v46, v47
	s_waitcnt vmcnt(3)
	v_mfma_f32_32x32x16_f16 v[66:81], v[18:21], v[30:33], 0
	global_load_dwordx4 v[18:21], v[152:153], off offset:2048
	v_cvt_pk_f16_f32 v3, v44, v45
	v_cvt_pk_f16_f32 v2, v42, v43
	ds_write_b128 v174, v[2:5] offset:32768
	v_cvt_pk_f16_f32 v57, v56, v57
	v_cvt_pk_f16_f32 v56, v54, v55
	v_cvt_pk_f16_f32 v55, v52, v53
	s_waitcnt vmcnt(3)
	v_mfma_f32_32x32x16_f16 v[66:81], v[22:25], v[86:89], v[66:81]
	global_load_dwordx4 v[22:25], v[152:153], off offset:3072
	v_cvt_pk_f16_f32 v54, v50, v51
	s_waitcnt vmcnt(1)
	v_mfma_f32_32x32x16_f16 v[66:81], v[26:29], v[18:21], v[66:81]
	v_lshl_add_u64 v[18:19], s[0:1], 0, v[154:155]
	v_add_co_u32_e32 v152, vcc, s23, v18
	s_nop 1
	v_addc_co_u32_e32 v153, vcc, 0, v19, vcc
	global_load_dwordx4 v[86:89], v[152:153], off offset:1024
	s_waitcnt vmcnt(1)
	v_mfma_f32_32x32x16_f16 v[66:81], v[82:85], v[22:25], v[66:81]
	v_cvt_pk_f16_f32 v85, v64, v65
	v_cvt_pk_f16_f32 v84, v62, v63
	v_cvt_pk_f16_f32 v83, v60, v61
	v_cvt_pk_f16_f32 v82, v58, v59
	v_mfma_f32_32x32x16_f16 v[18:33], v[54:57], v[126:129], 0
	s_nop 6
	v_cvt_pk_f16_f32 v73, v72, v73
	v_cvt_pk_f16_f32 v72, v70, v71
	v_cvt_pk_f16_f32 v70, v66, v67
	v_cvt_pk_f16_f32 v67, v76, v77
	v_cvt_pk_f16_f32 v66, v74, v75
	global_load_dwordx4 v[74:77], v154, s[0:1]
	ds_read_b128 v[2:5], v181
	ds_read_b128 v[6:9], v177
	ds_read_b128 v[10:13], v181 offset:32768
	global_load_dwordx4 v[14:17], v154, s[0:1] offset:2048
	global_load_dwordx4 v[34:37], v154, s[0:1] offset:3072
	v_mfma_f32_32x32x16_f16 v[50:65], v[54:57], v[110:113], 0
	v_cvt_pk_f16_f32 v71, v68, v69
	v_cvt_pk_f16_f32 v69, v80, v81
	v_cvt_pk_f16_f32 v68, v78, v79
	v_mfma_f32_32x32x16_f16 v[18:33], v[82:85], v[122:125], v[18:33]
	v_mfma_f32_32x32x16_f16 v[50:65], v[82:85], v[106:109], v[50:65]
	ds_read_b128 v[82:85], v177 offset:32768
	v_mfma_f32_32x32x16_f16 v[18:33], v[70:73], v[118:121], v[18:33]
	v_mfma_f32_32x32x16_f16 v[50:65], v[70:73], v[94:97], v[50:65]
	v_mfma_f32_32x32x16_f16 v[18:33], v[66:69], v[114:117], v[18:33]
	v_mfma_f32_32x32x16_f16 v[50:65], v[66:69], v[90:93], v[50:65]
	s_nop 10
	v_cvt_pk_f16_f32 v25, v24, v25
	v_cvt_pk_f16_f32 v24, v22, v23
	v_cvt_pk_f16_f32 v23, v20, v21
	v_cvt_pk_f16_f32 v22, v18, v19
	ds_write_b128 v132, v[22:25]
	s_waitcnt vmcnt(2) lgkmcnt(4)
	v_mfma_f32_32x32x16_f16 v[66:81], v[2:5], v[74:77], 0
	s_waitcnt lgkmcnt(3)
	v_mfma_f32_32x32x16_f16 v[66:81], v[6:9], v[182:185], v[66:81]
	s_waitcnt vmcnt(1) lgkmcnt(2)
	v_mfma_f32_32x32x16_f16 v[66:81], v[10:13], v[14:17], v[66:81]
	s_waitcnt vmcnt(0) lgkmcnt(1)
	v_mfma_f32_32x32x16_f16 v[66:81], v[82:85], v[34:37], v[66:81]
	v_mfma_f32_32x32x16_f16 v[34:49], v[2:5], v[168:171], 0
	global_load_dwordx4 v[2:5], v[152:153], off offset:2048
	s_nop 9
	v_cvt_pk_f16_f32 v73, v72, v73
	v_cvt_pk_f16_f32 v72, v70, v71
	v_cvt_pk_f16_f32 v71, v68, v69
	v_cvt_pk_f16_f32 v70, v66, v67
	v_cvt_pk_f16_f32 v69, v80, v81
	v_cvt_pk_f16_f32 v68, v78, v79
	v_mfma_f32_32x32x16_f16 v[34:49], v[6:9], v[86:89], v[34:49]
	global_load_dwordx4 v[6:9], v[152:153], off offset:3072
	v_cvt_pk_f16_f32 v67, v76, v77
	v_cvt_pk_f16_f32 v66, v74, v75
	s_waitcnt vmcnt(1)
	v_mfma_f32_32x32x16_f16 v[34:49], v[10:13], v[2:5], v[34:49]
	s_waitcnt vmcnt(0)
	v_mfma_f32_32x32x16_f16 v[34:49], v[82:85], v[6:9], v[34:49]
	v_mfma_f32_32x32x16_f16 v[2:17], v[70:73], v[126:129], 0
	s_nop 10
	v_cvt_pk_f16_f32 v41, v40, v41
	v_cvt_pk_f16_f32 v40, v38, v39
	v_cvt_pk_f16_f32 v38, v34, v35
	v_cvt_pk_f16_f32 v35, v44, v45
	v_cvt_pk_f16_f32 v34, v42, v43
	v_cvt_pk_f16_f32 v45, v32, v33
	v_cvt_pk_f16_f32 v44, v30, v31
	v_cvt_pk_f16_f32 v43, v28, v29
	v_cvt_pk_f16_f32 v42, v26, v27
	v_mfma_f32_32x32x16_f16 v[18:33], v[70:73], v[110:113], 0
	v_cvt_pk_f16_f32 v39, v36, v37
	v_cvt_pk_f16_f32 v37, v48, v49
	v_cvt_pk_f16_f32 v36, v46, v47
	ds_write_b128 v131, v[42:45]
	v_cvt_pk_f16_f32 v45, v56, v57
	v_cvt_pk_f16_f32 v44, v54, v55
	v_cvt_pk_f16_f32 v43, v52, v53
	v_mfma_f32_32x32x16_f16 v[2:17], v[66:69], v[122:125], v[2:17]
	v_cvt_pk_f16_f32 v42, v50, v51
	ds_write_b128 v132, v[42:45] offset:32768
	v_cvt_pk_f16_f32 v45, v64, v65
	v_cvt_pk_f16_f32 v44, v62, v63
	v_cvt_pk_f16_f32 v43, v60, v61
	v_cvt_pk_f16_f32 v42, v58, v59
	ds_write_b128 v131, v[42:45] offset:32768
	v_mfma_f32_32x32x16_f16 v[18:33], v[66:69], v[106:109], v[18:33]
	v_mfma_f32_32x32x16_f16 v[2:17], v[38:41], v[118:121], v[2:17]
	v_mfma_f32_32x32x16_f16 v[18:33], v[38:41], v[94:97], v[18:33]
	v_mfma_f32_32x32x16_f16 v[2:17], v[34:37], v[114:117], v[2:17]
	v_mfma_f32_32x32x16_f16 v[18:33], v[34:37], v[90:93], v[18:33]
	s_nop 10
	v_cvt_pk_f16_f32 v9, v8, v9
	v_cvt_pk_f16_f32 v8, v6, v7
	v_cvt_pk_f16_f32 v7, v4, v5
	v_cvt_pk_f16_f32 v6, v2, v3
	v_cvt_pk_f16_f32 v5, v16, v17
	v_cvt_pk_f16_f32 v4, v14, v15
	v_cvt_pk_f16_f32 v3, v12, v13
	v_cvt_pk_f16_f32 v2, v10, v11
	ds_write_b128 v135, v[6:9]
	ds_write_b128 v133, v[2:5]
	v_cvt_pk_f16_f32 v5, v24, v25
	v_cvt_pk_f16_f32 v4, v22, v23
	v_cvt_pk_f16_f32 v3, v20, v21
	v_cvt_pk_f16_f32 v2, v18, v19
	ds_write_b128 v135, v[2:5] offset:32768
	v_cvt_pk_f16_f32 v5, v32, v33
	v_cvt_pk_f16_f32 v4, v30, v31
	v_cvt_pk_f16_f32 v3, v28, v29
	v_cvt_pk_f16_f32 v2, v26, v27
	ds_write_b128 v133, v[2:5] offset:32768
	s_setprio 0
	s_waitcnt lgkmcnt(0)
	s_barrier
	ds_read_b64_tr_b16 v[2:3], v146
	ds_read_b64_tr_b16 v[4:5], v147
	ds_read_b64_tr_b16 v[36:37], v147 offset:32768
	ds_read_b64_tr_b16 v[34:35], v146 offset:32768
	ds_read_b64_tr_b16 v[18:19], v150
	ds_read_b64_tr_b16 v[20:21], v151
	ds_read_b64_tr_b16 v[40:41], v151 offset:32768
	ds_read_b64_tr_b16 v[38:39], v150 offset:32768
	s_waitcnt lgkmcnt(6)
	v_mfma_f32_32x32x16_f16 v[2:17], v[2:5], v[102:105], 0
	ds_read_b64_tr_b16 v[42:43], v148
	ds_read_b64_tr_b16 v[44:45], v149
	ds_read_b64_tr_b16 v[48:49], v149 offset:32768
	ds_read_b64_tr_b16 v[46:47], v148 offset:32768
	v_cmp_gt_u32_e64 s[0:1], 32, v167
	s_cmp_eq_u32 s5, 0
	v_cmp_lt_i32_e64 s[2:3], v162, v163
	s_waitcnt lgkmcnt(6)
	v_mfma_f32_32x32x16_f16 v[18:33], v[18:21], v[102:105], 0
	v_mfma_f32_32x32x16_f16 v[2:17], v[34:37], v[98:101], v[2:17]
	s_waitcnt lgkmcnt(4)
	v_mfma_f32_32x32x16_f16 v[18:33], v[38:41], v[98:101], v[18:33]
	s_nop 9
	v_mul_f32_e64 v34, v16, v16
	v_mul_f32_e64 v35, v17, v17
	v_mul_f32_e64 v36, v12, v12
	v_mul_f32_e64 v37, v13, v13
	v_mul_f32_e64 v50, v8, v8
	v_mul_f32_e64 v51, v9, v9
	v_pk_mul_f32 v[52:53], v[4:5], v[4:5]
	v_pk_fma_f32 v[50:51], v[6:7], v[6:7], v[50:51]
	v_pk_fma_f32 v[52:53], v[2:3], v[2:3], v[52:53]
	v_pk_fma_f32 v[36:37], v[10:11], v[10:11], v[36:37]
	v_pk_fma_f32 v[34:35], v[14:15], v[14:15], v[34:35]
	v_pk_mul_f32 v[116:117], v[24:25], v[24:25]
	v_pk_mul_f32 v[118:119], v[20:21], v[20:21]
	v_pk_add_f32 v[50:51], v[52:53], v[50:51]
	v_pk_add_f32 v[34:35], v[36:37], v[34:35]
	v_pk_mul_f32 v[112:113], v[32:33], v[32:33]
	v_pk_mul_f32 v[114:115], v[28:29], v[28:29]
	v_pk_mul_f32 v[120:121], v[18:19], v[18:19]
	v_pk_fma_f32 v[18:19], v[18:19], v[18:19], v[118:119]
	v_pk_fma_f32 v[20:21], v[22:23], v[22:23], v[116:117]
	v_pk_add_f32 v[34:35], v[50:51], v[34:35]
	v_pk_mul_f32 v[106:107], v[22:23], v[22:23]
	v_pk_add_f32 v[18:19], v[18:19], v[20:21]
	v_pk_fma_f32 v[20:21], v[26:27], v[26:27], v[114:115]
	v_pk_fma_f32 v[22:23], v[30:31], v[30:31], v[112:113]
	v_add_f32_e32 v34, v34, v35
	v_pk_add_f32 v[20:21], v[20:21], v[22:23]
	v_add_f32_e32 v36, 0, v34
	v_pk_mul_f32 v[108:109], v[26:27], v[26:27]
	v_pk_mul_f32 v[110:111], v[30:31], v[30:31]
	v_pk_add_f32 v[34:35], v[18:19], v[20:21]
	s_waitcnt lgkmcnt(2)
	v_mfma_f32_32x32x16_f16 v[18:33], v[42:45], v[102:105], 0
	v_add_f32_e32 v34, v34, v35
	v_add_f32_e32 v54, v36, v34
	v_sub_f32_e32 v55, v36, v34
	ds_read_b64_tr_b16 v[34:35], v144
	ds_read_b64_tr_b16 v[36:37], v145
	ds_read_b64_tr_b16 v[52:53], v145 offset:32768
	ds_read_b64_tr_b16 v[50:51], v144 offset:32768
	v_pk_fma_f32 v[4:5], v[4:5], v[4:5], v[118:119]
	v_pk_fma_f32 v[16:17], v[16:17], v[16:17], v[112:113]
	v_pk_fma_f32 v[14:15], v[14:15], v[14:15], v[110:111]
	s_waitcnt lgkmcnt(4)
	v_mfma_f32_32x32x16_f16 v[18:33], v[46:49], v[98:101], v[18:33]
	v_fma_f32 v12, v12, v12, v114
	v_fma_f32 v13, v13, v13, v115
	v_fma_f32 v10, v10, v10, v108
	v_fma_f32 v11, v11, v11, v109
	v_fma_f32 v8, v8, v8, v116
	v_fma_f32 v9, v9, v9, v117
	v_pk_fma_f32 v[6:7], v[6:7], v[6:7], v[106:107]
	v_pk_fma_f32 v[2:3], v[2:3], v[2:3], v[120:121]
	s_nop 3
	v_pk_mul_f32 v[38:39], v[32:33], v[32:33]
	v_pk_mul_f32 v[40:41], v[28:29], v[28:29]
	v_pk_mul_f32 v[42:43], v[24:25], v[24:25]
	v_pk_mul_f32 v[44:45], v[20:21], v[20:21]
	v_pk_fma_f32 v[42:43], v[22:23], v[22:23], v[42:43]
	v_pk_fma_f32 v[44:45], v[18:19], v[18:19], v[44:45]
	v_pk_fma_f32 v[40:41], v[26:27], v[26:27], v[40:41]
	v_pk_fma_f32 v[38:39], v[30:31], v[30:31], v[38:39]
	v_pk_add_f32 v[42:43], v[44:45], v[42:43]
	v_pk_add_f32 v[38:39], v[40:41], v[38:39]
	v_pk_fma_f32 v[4:5], v[20:21], v[20:21], v[4:5]
	v_pk_add_f32 v[38:39], v[42:43], v[38:39]
	v_pk_fma_f32 v[6:7], v[22:23], v[22:23], v[6:7]
	v_add_f32_e32 v56, v38, v39
	s_waitcnt lgkmcnt(2)
	v_mfma_f32_32x32x16_f16 v[34:49], v[34:37], v[102:105], 0
	v_add_f32_e32 v70, v54, v56
	v_add_f32_e32 v71, v55, v56
	v_sub_f32_e32 v72, v54, v56
	ds_read_b64_tr_b16 v[54:55], v142
	ds_read_b64_tr_b16 v[56:57], v143
	ds_read_b64_tr_b16 v[68:69], v143 offset:32768
	ds_read_b64_tr_b16 v[66:67], v142 offset:32768
	v_pk_fma_f32 v[8:9], v[24:25], v[24:25], v[8:9]
	v_pk_fma_f32 v[10:11], v[26:27], v[26:27], v[10:11]
	v_pk_fma_f32 v[12:13], v[28:29], v[28:29], v[12:13]
	s_waitcnt lgkmcnt(4)
	v_mfma_f32_32x32x16_f16 v[34:49], v[50:53], v[98:101], v[34:49]
	v_fma_f32 v14, v30, v30, v14
	v_fma_f32 v15, v31, v31, v15
	v_fma_f32 v16, v32, v32, v16
	v_fma_f32 v17, v33, v33, v17
	v_fma_f32 v2, v18, v18, v2
	v_fma_f32 v3, v19, v19, v3
	s_nop 5
	v_pk_mul_f32 v[50:51], v[48:49], v[48:49]
	v_pk_mul_f32 v[52:53], v[44:45], v[44:45]
	v_pk_mul_f32 v[58:59], v[40:41], v[40:41]
	v_pk_mul_f32 v[60:61], v[36:37], v[36:37]
	v_pk_fma_f32 v[58:59], v[38:39], v[38:39], v[58:59]
	v_pk_fma_f32 v[60:61], v[34:35], v[34:35], v[60:61]
	v_pk_fma_f32 v[52:53], v[42:43], v[42:43], v[52:53]
	v_pk_fma_f32 v[50:51], v[46:47], v[46:47], v[50:51]
	v_pk_add_f32 v[58:59], v[60:61], v[58:59]
	v_pk_add_f32 v[50:51], v[52:53], v[50:51]
	v_pk_fma_f32 v[4:5], v[36:37], v[36:37], v[4:5]
	v_pk_add_f32 v[50:51], v[58:59], v[50:51]
	v_pk_fma_f32 v[16:17], v[48:49], v[48:49], v[16:17]
	v_add_f32_e32 v73, v50, v51
	s_waitcnt lgkmcnt(2)
	v_mfma_f32_32x32x16_f16 v[50:65], v[54:57], v[102:105], 0
	v_add_f32_e32 v86, v70, v73
	v_sub_f32_e32 v87, v71, v73
	v_sub_f32_e32 v88, v72, v73
	ds_read_b64_tr_b16 v[70:71], v140
	ds_read_b64_tr_b16 v[72:73], v141
	ds_read_b64_tr_b16 v[84:85], v141 offset:32768
	ds_read_b64_tr_b16 v[82:83], v140 offset:32768
	v_pk_fma_f32 v[14:15], v[46:47], v[46:47], v[14:15]
	v_pk_fma_f32 v[12:13], v[44:45], v[44:45], v[12:13]
	v_pk_fma_f32 v[10:11], v[42:43], v[42:43], v[10:11]
	s_waitcnt lgkmcnt(4)
	v_mfma_f32_32x32x16_f16 v[50:65], v[66:69], v[98:101], v[50:65]
	v_fma_f32 v8, v40, v40, v8
	v_fma_f32 v9, v41, v41, v9
	v_fma_f32 v6, v38, v38, v6
	v_fma_f32 v7, v39, v39, v7
	v_fma_f32 v2, v34, v34, v2
	v_fma_f32 v3, v35, v35, v3
	s_nop 5
	v_pk_mul_f32 v[66:67], v[64:65], v[64:65]
	v_pk_mul_f32 v[68:69], v[60:61], v[60:61]
	v_pk_mul_f32 v[74:75], v[56:57], v[56:57]
	v_pk_mul_f32 v[76:77], v[52:53], v[52:53]
	v_pk_fma_f32 v[74:75], v[54:55], v[54:55], v[74:75]
	v_pk_fma_f32 v[76:77], v[50:51], v[50:51], v[76:77]
	v_pk_fma_f32 v[68:69], v[58:59], v[58:59], v[68:69]
	v_pk_fma_f32 v[66:67], v[62:63], v[62:63], v[66:67]
	v_pk_add_f32 v[74:75], v[76:77], v[74:75]
	v_pk_add_f32 v[66:67], v[68:69], v[66:67]
	v_pk_fma_f32 v[4:5], v[52:53], v[52:53], v[4:5]
	v_pk_add_f32 v[66:67], v[74:75], v[66:67]
	v_pk_fma_f32 v[6:7], v[54:55], v[54:55], v[6:7]
	v_add_f32_e32 v89, v66, v67
	s_waitcnt lgkmcnt(2)
	v_mfma_f32_32x32x16_f16 v[66:81], v[70:73], v[102:105], 0
	v_add_f32_e32 v94, v86, v89
	v_add_f32_e32 v126, v87, v89
	v_add_f32_e32 v127, v88, v89
	v_sub_f32_e32 v128, v86, v89
	ds_read_b64_tr_b16 v[86:87], v138
	ds_read_b64_tr_b16 v[88:89], v139
	ds_read_b64_tr_b16 v[124:125], v139 offset:32768
	ds_read_b64_tr_b16 v[122:123], v138 offset:32768
	v_pk_fma_f32 v[8:9], v[56:57], v[56:57], v[8:9]
	v_pk_fma_f32 v[10:11], v[58:59], v[58:59], v[10:11]
	s_waitcnt lgkmcnt(4)
	v_mfma_f32_32x32x16_f16 v[66:81], v[82:85], v[98:101], v[66:81]
	v_fma_f32 v12, v60, v60, v12
	v_fma_f32 v13, v61, v61, v13
	v_fma_f32 v14, v62, v62, v14
	v_fma_f32 v15, v63, v63, v15
	v_fma_f32 v16, v64, v64, v16
	v_fma_f32 v17, v65, v65, v17
	v_pk_fma_f32 v[2:3], v[50:51], v[50:51], v[2:3]
	s_nop 4
	v_pk_mul_f32 v[82:83], v[80:81], v[80:81]
	v_pk_mul_f32 v[84:85], v[76:77], v[76:77]
	v_pk_mul_f32 v[90:91], v[72:73], v[72:73]
	v_pk_mul_f32 v[92:93], v[68:69], v[68:69]
	v_pk_fma_f32 v[90:91], v[70:71], v[70:71], v[90:91]
	v_pk_fma_f32 v[92:93], v[66:67], v[66:67], v[92:93]
	v_pk_fma_f32 v[84:85], v[74:75], v[74:75], v[84:85]
	v_pk_fma_f32 v[82:83], v[78:79], v[78:79], v[82:83]
	v_pk_add_f32 v[90:91], v[92:93], v[90:91]
	v_pk_add_f32 v[82:83], v[84:85], v[82:83]
	v_pk_fma_f32 v[4:5], v[68:69], v[68:69], v[4:5]
	v_pk_add_f32 v[82:83], v[90:91], v[82:83]
	v_pk_fma_f32 v[18:19], v[80:81], v[80:81], v[16:17]
	v_add_f32_e32 v129, v82, v83
	v_add_f32_e32 v131, v94, v129
	s_waitcnt lgkmcnt(2)
	v_mfma_f32_32x32x16_f16 v[82:97], v[86:89], v[102:105], 0
	v_sub_f32_e32 v135, v126, v129
	v_add_f32_e32 v142, v127, v129
	v_sub_f32_e32 v143, v128, v129
	ds_read_b64_tr_b16 v[126:127], v136
	ds_read_b64_tr_b16 v[128:129], v137
	ds_read_b64_tr_b16 v[138:139], v137 offset:32768
	ds_read_b64_tr_b16 v[136:137], v136 offset:32768
	v_pk_fma_f32 v[20:21], v[78:79], v[78:79], v[14:15]
	v_pk_fma_f32 v[22:23], v[76:77], v[76:77], v[12:13]
	v_pk_fma_f32 v[24:25], v[74:75], v[74:75], v[10:11]
	s_waitcnt lgkmcnt(4)
	v_mfma_f32_32x32x16_f16 v[82:97], v[122:125], v[98:101], v[82:97]
	v_fma_f32 v26, v72, v72, v8
	v_fma_f32 v27, v73, v73, v9
	v_fma_f32 v28, v70, v70, v6
	v_fma_f32 v29, v71, v71, v7
	v_fma_f32 v30, v66, v66, v2
	v_fma_f32 v31, v67, v67, v3
	s_nop 5
	v_pk_fma_f32 v[32:33], v[84:85], v[84:85], v[4:5]
	s_waitcnt lgkmcnt(2)
	v_mfma_f32_32x32x16_f16 v[2:17], v[126:129], v[102:105], 0
	v_fma_f32 v28, v86, v86, v28
	v_fma_f32 v29, v87, v87, v29
	v_fma_f32 v24, v90, v90, v24
	v_fma_f32 v25, v91, v91, v25
	v_fma_f32 v22, v92, v92, v22
	v_fma_f32 v23, v93, v93, v23
	v_pk_fma_f32 v[20:21], v[94:95], v[94:95], v[20:21]
	v_pk_fma_f32 v[18:19], v[96:97], v[96:97], v[18:19]
	v_pk_fma_f32 v[30:31], v[82:83], v[82:83], v[30:31]
	v_pk_fma_f32 v[26:27], v[88:89], v[88:89], v[26:27]
	s_waitcnt lgkmcnt(0)
	v_mfma_f32_32x32x16_f16 v[2:17], v[136:139], v[98:101], v[2:17]
	v_mul_f32_e64 v122, v96, v96
	v_mul_f32_e64 v123, v97, v97
	v_mul_f32_e64 v124, v92, v92
	v_mul_f32_e64 v125, v93, v93
	v_mul_f32_e64 v132, v88, v88
	v_mul_f32_e64 v133, v89, v89
	v_pk_mul_f32 v[140:141], v[84:85], v[84:85]
	v_pk_fma_f32 v[132:133], v[86:87], v[86:87], v[132:133]
	v_pk_fma_f32 v[140:141], v[82:83], v[82:83], v[140:141]
	v_pk_fma_f32 v[124:125], v[90:91], v[90:91], v[124:125]
	s_nop 1
	v_pk_mul_f32 v[38:39], v[8:9], v[8:9]
	v_pk_mul_f32 v[40:41], v[4:5], v[4:5]
	v_pk_mul_f32 v[34:35], v[16:17], v[16:17]
	v_pk_mul_f32 v[36:37], v[12:13], v[12:13]
	v_pk_fma_f32 v[16:17], v[16:17], v[16:17], v[18:19]
	v_pk_fma_f32 v[18:19], v[14:15], v[14:15], v[20:21]
	v_pk_fma_f32 v[12:13], v[12:13], v[12:13], v[22:23]
	v_pk_fma_f32 v[20:21], v[10:11], v[10:11], v[24:25]
	v_pk_fma_f32 v[22:23], v[6:7], v[6:7], v[28:29]
	v_pk_fma_f32 v[24:25], v[2:3], v[2:3], v[30:31]
	v_pk_fma_f32 v[2:3], v[2:3], v[2:3], v[40:41]
	v_pk_fma_f32 v[6:7], v[6:7], v[6:7], v[38:39]
	v_pk_fma_f32 v[4:5], v[4:5], v[4:5], v[32:33]
	v_pk_add_f32 v[2:3], v[2:3], v[6:7]
	v_pk_fma_f32 v[6:7], v[10:11], v[10:11], v[36:37]
	v_pk_fma_f32 v[10:11], v[14:15], v[14:15], v[34:35]
	v_pk_fma_f32 v[8:9], v[8:9], v[8:9], v[26:27]
	v_pk_add_f32 v[6:7], v[6:7], v[10:11]
	v_sub_f32_e32 v10, v24, v25
	v_add_f32_e32 v11, v25, v24
	v_add_f32_e32 v10, v4, v10
	v_sub_f32_e32 v14, v11, v4
	v_add_f32_e32 v4, v4, v11
	v_sub_f32_e32 v10, v10, v5
	v_sub_f32_e32 v11, v14, v5
	v_add_f32_e32 v4, v5, v4
	v_add_f32_e32 v5, v22, v10
	v_add_f32_e32 v10, v22, v11
	v_sub_f32_e32 v11, v4, v22
	v_add_f32_e32 v4, v22, v4
	v_sub_f32_e32 v5, v5, v23
	v_add_f32_e32 v10, v23, v10
	v_sub_f32_e32 v11, v11, v23
	v_add_f32_e32 v4, v23, v4
	v_add_f32_e32 v5, v8, v5
	v_sub_f32_e32 v10, v10, v8
	v_sub_f32_e32 v11, v11, v8
	v_add_f32_e32 v4, v8, v4
	v_sub_f32_e32 v5, v5, v9
	v_pk_fma_f32 v[122:123], v[94:95], v[94:95], v[122:123]
	v_sub_f32_e32 v8, v10, v9
	v_sub_f32_e32 v10, v11, v9
	v_add_f32_e32 v4, v9, v4
	v_add_f32_e32 v5, v20, v5
	v_pk_add_f32 v[132:133], v[140:141], v[132:133]
	v_pk_add_f32 v[122:123], v[124:125], v[122:123]
	v_add_f32_e32 v8, v20, v8
	v_add_f32_e32 v9, v20, v10
	v_sub_f32_e32 v4, v4, v20
	v_sub_f32_e32 v5, v5, v21
	v_pk_add_f32 v[122:123], v[132:133], v[122:123]
	v_add_f32_e32 v8, v21, v8
	v_add_f32_e32 v9, v21, v9
	v_sub_f32_e32 v4, v4, v21
	v_add_f32_e32 v5, v12, v5
	v_add_f32_e32 v122, v122, v123
	v_pk_add_f32 v[2:3], v[2:3], v[6:7]
	v_sub_f32_e32 v8, v8, v12
	v_add_f32_e32 v9, v12, v9
	v_sub_f32_e32 v4, v4, v12
	v_sub_f32_e32 v5, v5, v13
	v_add_f32_e32 v123, v131, v122
	v_add_f32_e32 v2, v2, v3
	v_sub_f32_e32 v8, v8, v13
	v_add_f32_e32 v9, v13, v9
	v_sub_f32_e32 v4, v4, v13
	v_add_f32_e32 v5, v18, v5
	v_add_f32_e32 v3, v123, v2
	v_add_f32_e32 v8, v18, v8
	v_sub_f32_e32 v9, v9, v18
	v_sub_f32_e32 v4, v4, v18
	v_sub_f32_e32 v5, v5, v19
	v_and_b32_e32 v10, 8, v156
	v_add_f32_e32 v8, v19, v8
	v_sub_f32_e32 v9, v9, v19
	v_sub_f32_e32 v4, v4, v19
	v_add_f32_e32 v5, v16, v5
	v_cmp_eq_u32_e32 vcc, 0, v10
	v_cndmask_b32_e64 v10, -v3, v3, s[0:1]
	s_cselect_b64 s[0:1], -1, 0
	s_bitcmp0_b32 s4, 7
	v_sub_f32_e32 v8, v8, v16
	v_sub_f32_e32 v9, v9, v16
	v_sub_f32_e32 v4, v4, v16
	v_sub_f32_e32 v5, v5, v17
	v_cndmask_b32_e64 v11, -v3, v3, s[0:1]
	s_cselect_b64 s[0:1], -1, 0
	v_and_b32_e32 v16, 32, v156
	v_sub_f32_e32 v8, v8, v17
	v_cndmask_b32_e64 v5, -v5, v5, vcc
	v_cndmask_b32_e64 v12, -v3, v3, s[0:1]
	v_cndmask_b32_e64 v18, v161, v162, s[2:3]
	v_cmp_eq_u32_e64 s[2:3], 0, v16
	v_lshlrev_b32_e32 v18, 2, v18
	v_cmp_eq_u32_e64 s[0:1], 0, v134
	v_cndmask_b32_e64 v16, v11, v5, s[2:3]
	v_cndmask_b32_e64 v5, v5, v11, s[2:3]
	v_cndmask_b32_e64 v11, v8, v12, s[2:3]
	ds_bpermute_b32 v11, v18, v11
	v_and_b32_e32 v14, 2, v156
	v_cndmask_b32_e64 v13, -v3, v3, s[0:1]
	v_cmp_eq_u32_e64 s[0:1], 0, v14
	v_cndmask_b32_e64 v8, v12, v8, s[2:3]
	v_add_f32_e32 v124, v135, v122
	v_cndmask_b32_e64 v14, -v3, v3, s[0:1]
	v_cmp_eq_u32_e64 s[0:1], 0, v130
	v_sub_f32_e32 v4, v4, v17
	s_waitcnt lgkmcnt(0)
	v_add_f32_e32 v8, v8, v11
	v_cndmask_b32_e64 v15, -v3, v3, s[0:1]
	v_cndmask_b32_e64 v11, v14, v10, s[2:3]
	v_cndmask_b32_e64 v10, v10, v14, s[2:3]
	v_sub_f32_e32 v6, v124, v2
	v_sub_f32_e32 v9, v9, v17
	v_cndmask_b32_e64 v3, -v3, v3, vcc
	ds_bpermute_b32 v10, v18, v10
	v_cndmask_b32_e64 v12, v4, v15, s[2:3]
	v_sub_f32_e32 v125, v142, v122
	v_cndmask_b32_e64 v19, v9, v13, s[2:3]
	v_cndmask_b32_e64 v9, v13, v9, s[2:3]
	ds_bpermute_b32 v12, v18, v12
	v_cndmask_b32_e64 v13, v6, v3, s[2:3]
	v_sub_f32_e32 v7, v125, v2
	v_bfe_i32 v17, v156, 5, 1
	ds_bpermute_b32 v5, v18, v5
	ds_bpermute_b32 v13, v18, v13
	v_sub_f32_e32 v122, v143, v122
	v_cndmask_b32_e64 v3, v3, v6, s[2:3]
	v_and_b32_e32 v6, v17, v7
	v_sub_f32_e32 v2, v122, v2
	ds_bpermute_b32 v19, v18, v19
	ds_bpermute_b32 v6, v18, v6
	s_waitcnt lgkmcnt(5)
	v_add_f32_e32 v10, v11, v10
	v_cndmask_b32_e64 v4, v15, v4, s[2:3]
	v_and_b32_e32 v11, v17, v2
	s_waitcnt lgkmcnt(4)
	v_add_f32_e32 v4, v4, v12
	ds_bpermute_b32 v11, v18, v11
	v_and_b32_e32 v12, 16, v156
	v_cmp_lt_i32_e64 s[4:5], v164, v163
	s_waitcnt lgkmcnt(4)
	v_add_f32_e32 v5, v16, v5
	s_waitcnt lgkmcnt(3)
	v_add_f32_e32 v3, v3, v13
	v_cndmask_b32_e64 v13, v161, v164, s[4:5]
	v_cmp_eq_u32_e64 s[4:5], 0, v12
	s_waitcnt lgkmcnt(2)
	v_add_f32_e32 v9, v9, v19
	v_lshlrev_b32_e32 v13, 2, v13
	v_cndmask_b32_e64 v12, v4, v5, s[4:5]
	v_cndmask_b32_e64 v4, v5, v4, s[4:5]
	v_cndmask_b32_e64 v5, 0, v7, s[2:3]
	s_waitcnt lgkmcnt(1)
	v_add_f32_e32 v5, v5, v6
	v_cndmask_b32_e64 v2, 0, v2, s[2:3]
	v_cndmask_b32_e64 v7, v9, v5, s[4:5]
	ds_bpermute_b32 v4, v13, v4
	s_waitcnt lgkmcnt(1)
	v_add_f32_e32 v2, v2, v11
	v_cndmask_b32_e64 v6, v3, v8, s[4:5]
	v_cndmask_b32_e64 v3, v8, v3, s[4:5]
	ds_bpermute_b32 v7, v13, v7
	ds_bpermute_b32 v3, v13, v3
	v_cndmask_b32_e64 v8, v10, v2, s[4:5]
	ds_bpermute_b32 v8, v13, v8
	v_cndmask_b32_e64 v5, v5, v9, s[4:5]
	s_waitcnt lgkmcnt(3)
	v_add_f32_e32 v4, v12, v4
	s_waitcnt lgkmcnt(2)
	v_add_f32_e32 v5, v5, v7
	s_waitcnt lgkmcnt(1)
	v_add_f32_e32 v3, v6, v3
	v_cndmask_b32_e64 v2, v2, v10, s[4:5]
	v_cndmask_b32_e32 v6, v5, v4, vcc
	v_cndmask_b32_e32 v4, v4, v5, vcc
	v_mov_b32_e32 v5, v155
	s_waitcnt lgkmcnt(0)
	v_add_f32_e32 v2, v2, v8
	v_mov_b32_dpp v5, v4 row_mirror row_mask:0xf bank_mask:0xf
	s_nop 1
	v_add_f32_dpp v4, v5, v6 row_half_mirror row_mask:0xf bank_mask:0xf bound_ctrl:1
	v_cndmask_b32_e32 v5, v2, v3, vcc
	v_cndmask_b32_e32 v2, v3, v2, vcc
	v_mov_b32_e32 v3, v155
	s_nop 1
	v_mov_b32_dpp v3, v2 row_mirror row_mask:0xf bank_mask:0xf
	s_nop 1
	v_add_f32_dpp v2, v3, v5 row_half_mirror row_mask:0xf bank_mask:0xf bound_ctrl:1
	v_cndmask_b32_e64 v3, v2, v4, s[0:1]
	v_cndmask_b32_e64 v2, v4, v2, s[0:1]
	v_mov_b32_e32 v4, v155
	s_nop 1
	v_mov_b32_dpp v4, v2 row_half_mirror row_mask:0xf bank_mask:0xf
	s_nop 1
	v_add_f32_dpp v2, v4, v3 quad_perm:[3,2,1,0] row_mask:0xf bank_mask:0xf bound_ctrl:1
	v_and_b32_e32 v4, 3, v156
	v_cmp_eq_u32_e32 vcc, 0, v4
	v_and_b32_e32 v4, 56, v156
	v_add_f32_dpp v2, v2, v2 quad_perm:[2,3,0,1] row_mask:0xf bank_mask:0xf bound_ctrl:1
	v_mov_b32_e32 v3, 0
	v_cmp_ne_u32_e64 s[0:1], 56, v4
	s_and_b64 s[2:3], vcc, s[0:1]
	v_mov_b32_dpp v3, v2 quad_perm:[1,0,3,2] row_mask:0xf bank_mask:0xf
	s_and_saveexec_b64 s[0:1], s[2:3]
	v_and_b32_e32 v4, 0xfc, v156
	v_add_f32_e32 v2, v2, v3
	v_or_b32_e32 v4, v165, v4
	ds_write_b32 v4, v2
	s_or_b64 exec, exec, s[0:1]
	v_cmp_gt_i32_e32 vcc, 14, v156
	s_waitcnt lgkmcnt(0)
	s_barrier
	s_and_saveexec_b64 s[0:1], vcc
	s_cbranch_execz .LBB1_2
	ds_read_b32 v2, v166
	ds_read_b32 v3, v166 offset:64
	ds_read_b32 v4, v166 offset:128
	ds_read_b32 v5, v166 offset:192
	s_waitcnt lgkmcnt(2)
	v_add_f32_e32 v2, v2, v3
	s_waitcnt lgkmcnt(1)
	v_add_f32_e32 v2, v2, v4
	s_waitcnt lgkmcnt(0)
	v_add_f32_e32 v2, v2, v5
	v_mul_f32_e32 v4, 0x39800000, v2
	v_lshl_add_u64 v[2:3], v[156:157], 2, s[14:15]
	global_store_dword v[2:3], v4, off
	s_branch .LBB1_2

	.amdhsa_kernel _Z9qsim_mainPKDF16_PK15HIP_vector_typeIfLj2EEPf
		.amdhsa_group_segment_fixed_size 68352
		.amdhsa_private_segment_fixed_size 0
		.amdhsa_kernarg_size 24
		.amdhsa_user_sgpr_count 2
		.amdhsa_user_sgpr_dispatch_ptr 0
		.amdhsa_user_sgpr_queue_ptr 0
		.amdhsa_user_sgpr_kernarg_segment_ptr 1
		.amdhsa_user_sgpr_dispatch_id 0
		.amdhsa_user_sgpr_kernarg_preload_length 0
		.amdhsa_user_sgpr_kernarg_preload_offset 0
		.amdhsa_user_sgpr_private_segment_size 0
		.amdhsa_uses_dynamic_stack 0
		.amdhsa_enable_private_segment 0
		.amdhsa_system_sgpr_workgroup_id_x 1
		.amdhsa_system_sgpr_workgroup_id_y 0
		.amdhsa_system_sgpr_workgroup_id_z 0
		.amdhsa_system_sgpr_workgroup_info 0
		.amdhsa_system_vgpr_workitem_id 0
		.amdhsa_next_free_vgpr 190
		.amdhsa_next_free_sgpr 96
		.amdhsa_accum_offset 192
		.amdhsa_reserve_vcc 1
		.amdhsa_float_round_mode_32 0
		.amdhsa_float_round_mode_16_64 0
		.amdhsa_float_denorm_mode_32 3
		.amdhsa_float_denorm_mode_16_64 3
		.amdhsa_dx10_clamp 1
		.amdhsa_ieee_mode 1
		.amdhsa_fp16_overflow 0
		.amdhsa_tg_split 0
		.amdhsa_exception_fp_ieee_invalid_op 0
		.amdhsa_exception_fp_denorm_src 0
		.amdhsa_exception_fp_ieee_div_zero 0
		.amdhsa_exception_fp_ieee_overflow 0
		.amdhsa_exception_fp_ieee_underflow 0
		.amdhsa_exception_fp_ieee_inexact 0
		.amdhsa_exception_int_div_zero 0
	.end_amdhsa_kernel

amdhsa.kernels:
  - .agpr_count:     0
    .args:
      - .actual_access:  read_only
        .address_space:  global
        .offset:         0
        .size:           8
        .value_kind:     global_buffer
      - .actual_access:  read_only
        .address_space:  global
        .offset:         8
        .size:           8
        .value_kind:     global_buffer
      - .actual_access:  read_only
        .address_space:  global
        .offset:         16
        .size:           8
        .value_kind:     global_buffer
      - .actual_access:  read_only
        .address_space:  global
        .offset:         24
        .size:           8
        .value_kind:     global_buffer
      - .actual_access:  write_only
        .address_space:  global
        .offset:         32
        .size:           8
        .value_kind:     global_buffer
      - .actual_access:  write_only
        .address_space:  global
        .offset:         40
        .size:           8
        .value_kind:     global_buffer
    .group_segment_fixed_size: 1920
    .kernarg_segment_align: 8
    .kernarg_segment_size: 48
    .language:       OpenCL C
    .language_version:
      - 2
      - 0
    .max_flat_workgroup_size: 256
    .name:           _Z11prep_kernelPKfS0_S0_S0_PDF16_P15HIP_vector_typeIfLj2EE
    .private_segment_fixed_size: 0
    .sgpr_count:     22
    .sgpr_spill_count: 0
    .symbol:         _Z11prep_kernelPKfS0_S0_S0_PDF16_P15HIP_vector_typeIfLj2EE.kd
    .uniform_work_group_size: 1
    .uses_dynamic_stack: false
    .vgpr_count:     59
    .vgpr_spill_count: 0
    .wavefront_size: 64
  - .agpr_count:     0
    .args:
      - .actual_access:  read_only
        .address_space:  global
        .offset:         0
        .size:           8
        .value_kind:     global_buffer
      - .actual_access:  read_only
        .address_space:  global
        .offset:         8
        .size:           8
        .value_kind:     global_buffer
      - .actual_access:  write_only
        .address_space:  global
        .offset:         16
        .size:           8
        .value_kind:     global_buffer
    .group_segment_fixed_size: 68352
    .kernarg_segment_align: 8
    .kernarg_segment_size: 24
    .language:       OpenCL C
    .language_version:
      - 2
      - 0
    .max_flat_workgroup_size: 256
    .name:           _Z9qsim_mainPKDF16_PK15HIP_vector_typeIfLj2EEPf
    .private_segment_fixed_size: 0
    .sgpr_count:     41
    .sgpr_spill_count: 0
    .symbol:         _Z9qsim_mainPKDF16_PK15HIP_vector_typeIfLj2EEPf.kd
    .uniform_work_group_size: 1
    .uses_dynamic_stack: false
    .vgpr_count:     190
    .vgpr_spill_count: 0
    .wavefront_size: 64
